# v47 + per-unit accumulator clearing removed: first K iteration of every GEMM unit peeled, first MFMA of each accumulator uses srcC=0 (6 GEMM bodies)
# baseline (speedup 1.0000x reference)
; #define PG8_STAGE(bufoff, gbase, voff) do { _Pragma("unroll") for (int _i = 0; _i < 2; ++_i) \
;         __builtin_amdgcn_global_load_lds((const unsigned*)((const char*)(gbase) + (voff)[_i]), (PG8_LAS unsigned*)(lds + (bufoff) + ldsw + _i * 8192), 16, 0, 0); } while (0)
; #define PG8_LDA(dst, b, h) do { _Pragma("unroll") for (int m = 0; m < 4; ++m) _Pragma("unroll") for (int k = 0; k < 2; ++k) dst[m][k] = *(const PG8_LAS bf16x8*)(lds + PG8_SA(b, h) + aoff + m * 2048 + k * 1024); } while (0)
; #define PG8_LDB(dst, b, h) do { _Pragma("unroll") for (int n = 0; n < 2; ++n) _Pragma("unroll") for (int k = 0; k < 2; ++k) dst[n][k] = *(const PG8_LAS bf16x8*)(lds + PG8_SB(b, h) + boff + n * 2048 + k * 1024); } while (0)
; #define PG8_WAIT_V(n) asm volatile("s_waitcnt vmcnt(" #n ")" ::: "memory")
; #define PG8_WAIT_L(n) asm volatile("s_waitcnt lgkmcnt(" #n ")" ::: "memory")
; #define PG8_BAR __builtin_amdgcn_s_barrier()
; #define PG8_SCHED __builtin_amdgcn_sched_barrier(0)
; #define PG8_WAIT_V(n) asm volatile("s_waitcnt vmcnt(" #n ")" ::: "memory")
; template <class Epi, class Sched, bool ALIGN_EPI = false, bool SP2 = false>
; __device__ __forceinline__ void gemm_phase(PG8_LAS unsigned char* lds, const Gemm g, const Sched& S, const Epi& E, const int tid) {
;     ...
;         const bool has_next = S.next(ui + 1, nxt);
;         const char* nA = has_next ? (const char*)g.A + (size_t)nxt.pm * tstep + (size_t)nxt.k0 * 2 : cA; const char* nB = has_next ? (const char*)g.Bt + (size_t)nxt.pn * tstep + (size_t)nxt.k0 * 2 : cB;
;         for (int t = 0; t < nt; t += 2) {
;             const bool last = (t == nt - 2);
;             const char* a1 = cA + (size_t)(t + 1) * kstep;
;             const char* a2 = last ? nA : cA + (size_t)(t + 2) * kstep; const char* b2 = last ? nB : cB + (size_t)(t + 2) * kstep;
;             const char* a3 = a2 + kstep; const char* b3 = b2 + kstep;
;             if (last && has_next) S.a_ready(nxt);
;             if constexpr (SP2) {
;             PG8_LDB(B0, 0, 0); PG8_LDB(B1, 0, 1); PG8_SCHED; PG8_LDA(At, 0, 0); PG8_STAGE(PG8_SA(1, 1), a1 + hstep, voffA);
;             PG8_WAIT_V(8); PG8_WAIT_L(0); PG8_BAR; PG8_MMA(0, 0, At, B0); PG8_MMA(0, 1, At, B1); PG8_BAR; PG8_SCHED;
;             PG8_LDA(At, 0, 1); PG8_STAGE(PG8_SB(0, 0), b2, voffB); PG8_STAGE(PG8_SB(0, 1), b2 + hstep, voffB); PG8_STAGE(PG8_SA(0, 0), a2, voffA);
.LBB0_756:
	s_ashr_i32 s75, s74, 31
	s_lshl_b64 s[10:11], s[74:75], 20
	s_add_u32 s78, s59, s10
	s_addc_u32 s79, s31, s11
	s_and_b64 s[10:11], s[76:77], exec
	s_cselect_b32 s1, s79, s41
	s_cselect_b32 s2, s78, s40
	s_ashr_i32 s73, s72, 31
	s_lshl_b64 s[10:11], s[72:73], 20
	s_add_u32 s80, s48, s10
	s_addc_u32 s81, s27, s11
	s_and_b64 s[10:11], s[76:77], exec
	s_cselect_b32 s5, s81, s7
	s_cselect_b32 s10, s80, s6
	s_add_u32 s40, s40, 0x80080
	s_addc_u32 s41, s41, 0
	s_add_u32 s11, s6, 0x100
	s_waitcnt vmcnt(0)
	v_mov_b32_e32 v2, 0
	s_addc_u32 s12, s7, 0
	s_mov_b32 s13, -2
	s_add_u32 s6, s40, 0xfff80080
	s_addc_u32 s7, s41, -1
	s_add_i32 s15, 0, 0x10000
	s_cmp_eq_u32 s13, 28
	s_cselect_b32 s69, s1, s7
	s_cselect_b32 s68, s2, s6
	v_add_u32_e32 v131, s15, v152
	s_cselect_b32 s7, s5, s12
	s_cselect_b32 s6, s10, s11
	s_add_i32 s16, 0, 0x14000
	ds_read_b128 v[164:167], v131
	ds_read_b128 v[168:171], v131 offset:1024
	ds_read_b128 v[172:175], v131 offset:2048
	ds_read_b128 v[176:179], v131 offset:3072
	v_add_u32_e32 v131, s16, v152
	ds_read_b128 v[180:183], v131
	ds_read_b128 v[184:187], v131 offset:1024
	ds_read_b128 v[188:191], v131 offset:2048
	ds_read_b128 v[192:195], v131 offset:3072
	v_lshl_add_u64 v[132:133], s[40:41], 0, v[144:145]
	s_add_i32 m0, s46, 0xc000
	ds_read_b128 v[198:201], v163
	ds_read_b128 v[202:205], v163 offset:1024
	ds_read_b128 v[206:209], v163 offset:2048
	ds_read_b128 v[210:213], v163 offset:3072
	ds_read_b128 v[214:217], v163 offset:4096
	ds_read_b128 v[218:221], v163 offset:5120
	ds_read_b128 v[222:225], v163 offset:6144
	ds_read_b128 v[226:229], v163 offset:7168
	global_load_lds_dwordx4 v[132:133], off
	v_lshl_add_u64 v[132:133], s[40:41], 0, v[146:147]
	s_add_i32 m0, s46, 0xe000
	s_nop 0
	global_load_lds_dwordx4 v[132:133], off
	s_waitcnt vmcnt(8)
	s_waitcnt lgkmcnt(0)
	s_barrier
	s_setprio 1
	s_waitcnt lgkmcnt(0)
	v_mfma_f32_16x16x32_bf16 v[126:129], v[164:167], v[198:201], 0
	v_mfma_f32_16x16x32_bf16 v[122:125], v[172:175], v[198:201], 0
	v_mfma_f32_16x16x32_bf16 v[118:121], v[164:167], v[206:209], 0
	v_mfma_f32_16x16x32_bf16 v[110:113], v[172:175], v[206:209], 0
	v_mfma_f32_16x16x32_bf16 v[102:105], v[164:167], v[214:217], 0
	v_mfma_f32_16x16x32_bf16 v[94:97], v[172:175], v[214:217], 0
	v_mfma_f32_16x16x32_bf16 v[86:89], v[164:167], v[222:225], 0
	v_mfma_f32_16x16x32_bf16 v[78:81], v[172:175], v[222:225], 0
	v_mfma_f32_16x16x32_bf16 v[126:129], v[168:171], v[202:205], v[126:129]
	v_mfma_f32_16x16x32_bf16 v[122:125], v[176:179], v[202:205], v[122:125]
	v_mfma_f32_16x16x32_bf16 v[118:121], v[168:171], v[210:213], v[118:121]
	v_mfma_f32_16x16x32_bf16 v[110:113], v[176:179], v[210:213], v[110:113]
	v_mfma_f32_16x16x32_bf16 v[102:105], v[168:171], v[218:221], v[102:105]
	v_mfma_f32_16x16x32_bf16 v[94:97], v[176:179], v[218:221], v[94:97]
	v_mfma_f32_16x16x32_bf16 v[86:89], v[168:171], v[226:229], v[86:89]
	v_mfma_f32_16x16x32_bf16 v[78:81], v[176:179], v[226:229], v[78:81]
	s_setprio 0
	s_setprio 1
	v_mfma_f32_16x16x32_bf16 v[114:117], v[180:183], v[198:201], 0
	v_mfma_f32_16x16x32_bf16 v[106:109], v[188:191], v[198:201], 0
	v_mfma_f32_16x16x32_bf16 v[98:101], v[180:183], v[206:209], 0
	v_mfma_f32_16x16x32_bf16 v[90:93], v[188:191], v[206:209], 0
	v_mfma_f32_16x16x32_bf16 v[82:85], v[180:183], v[214:217], 0
	v_mfma_f32_16x16x32_bf16 v[74:77], v[188:191], v[214:217], 0
	v_mfma_f32_16x16x32_bf16 v[70:73], v[180:183], v[222:225], 0
	v_mfma_f32_16x16x32_bf16 v[66:69], v[188:191], v[222:225], 0
	v_mfma_f32_16x16x32_bf16 v[114:117], v[184:187], v[202:205], v[114:117]
	v_mfma_f32_16x16x32_bf16 v[106:109], v[192:195], v[202:205], v[106:109]
	v_mfma_f32_16x16x32_bf16 v[98:101], v[184:187], v[210:213], v[98:101]
	v_mfma_f32_16x16x32_bf16 v[90:93], v[192:195], v[210:213], v[90:93]
	v_mfma_f32_16x16x32_bf16 v[82:85], v[184:187], v[218:221], v[82:85]
	v_mfma_f32_16x16x32_bf16 v[74:77], v[192:195], v[218:221], v[74:77]
	v_mfma_f32_16x16x32_bf16 v[70:73], v[184:187], v[226:229], v[70:73]
	v_mfma_f32_16x16x32_bf16 v[66:69], v[192:195], v[226:229], v[66:69]
	s_setprio 0
	s_barrier
	s_add_i32 s15, s15, s49
	v_lshl_add_u64 v[132:133], s[6:7], 0, v[136:137]
	s_mov_b32 m0, s15
	ds_read_b128 v[198:201], v163 offset:16384
	ds_read_b128 v[202:205], v163 offset:17408
	ds_read_b128 v[206:209], v163 offset:18432
	ds_read_b128 v[210:213], v163 offset:19456
	ds_read_b128 v[214:217], v163 offset:20480
	ds_read_b128 v[218:221], v163 offset:21504
	ds_read_b128 v[222:225], v163 offset:22528
	ds_read_b128 v[226:229], v163 offset:23552
	global_load_lds_dwordx4 v[132:133], off
	s_add_i32 m0, s15, 0x2000
	s_add_u32 s18, s6, 0x80000
	v_lshl_add_u64 v[148:149], s[6:7], 0, v[140:141]
	s_addc_u32 s19, s7, 0
	s_add_i32 s15, s16, s49
	global_load_lds_dwordx4 v[148:149], off
	v_lshl_add_u64 v[230:231], s[18:19], 0, v[136:137]
	s_mov_b32 m0, s15
	v_lshl_add_u64 v[242:243], s[68:69], 0, v[138:139]
	global_load_lds_dwordx4 v[230:231], off
	v_lshl_add_u64 v[230:231], s[18:19], 0, v[140:141]
	s_add_i32 m0, s15, 0x2000
	s_nop 0
	global_load_lds_dwordx4 v[230:231], off
	v_lshl_add_u64 v[230:231], s[68:69], 0, v[134:135]
	s_mov_b32 m0, s46
	s_nop 0
	global_load_lds_dwordx4 v[230:231], off
	s_mov_b32 m0, s47
	s_nop 0
	global_load_lds_dwordx4 v[242:243], off
	s_waitcnt vmcnt(8)
	s_waitcnt lgkmcnt(0)
	s_barrier
; #define PG8_STAGE(bufoff, gbase, voff) do { _Pragma("unroll") for (int _i = 0; _i < 2; ++_i) \
;         __builtin_amdgcn_global_load_lds((const unsigned*)((const char*)(gbase) + (voff)[_i]), (PG8_LAS unsigned*)(lds + (bufoff) + ldsw + _i * 8192), 16, 0, 0); } while (0)
; #define PG8_LDA(dst, b, h) do { _Pragma("unroll") for (int m = 0; m < 4; ++m) _Pragma("unroll") for (int k = 0; k < 2; ++k) dst[m][k] = *(const PG8_LAS bf16x8*)(lds + PG8_SA(b, h) + aoff + m * 2048 + k * 1024); } while (0)
; #define PG8_LDB(dst, b, h) do { _Pragma("unroll") for (int n = 0; n < 2; ++n) _Pragma("unroll") for (int k = 0; k < 2; ++k) dst[n][k] = *(const PG8_LAS bf16x8*)(lds + PG8_SB(b, h) + boff + n * 2048 + k * 1024); } while (0)
; #define PG8_MMA(ai, bj, At, Bt) do { __builtin_amdgcn_s_setprio(1); _Pragma("unroll") for (int m = 0; m < 4; ++m) _Pragma("unroll") for (int n = 0; n < 2; ++n) _Pragma("unroll") for (int k = 0; k < 2; ++k) \
;         acc[ai][bj][m][n] = __builtin_amdgcn_mfma_f32_16x16x32_bf16(Bt[n][k], At[m][k], acc[ai][bj][m][n], 0, 0, 0); __builtin_amdgcn_s_setprio(0); } while (0)
; #define PG8_WAIT_V(n) asm volatile("s_waitcnt vmcnt(" #n ")" ::: "memory")
; #define PG8_WAIT_L(n) asm volatile("s_waitcnt lgkmcnt(" #n ")" ::: "memory")
; #define PG8_BAR __builtin_amdgcn_s_barrier()
; #define PG8_SCHED __builtin_amdgcn_sched_barrier(0)
; #define PG8_STAGE(bufoff, gbase, voff) do { _Pragma("unroll") for (int _i = 0; _i < 2; ++_i) \
;         __builtin_amdgcn_global_load_lds((const unsigned*)((const char*)(gbase) + (voff)[_i]), (PG8_LAS unsigned*)(lds + (bufoff) + ldsw + _i * 8192), 16, 0, 0); } while (0)
; #define PG8_WAIT_V(n) asm volatile("s_waitcnt vmcnt(" #n ")" ::: "memory")
; #define PG8_WAIT_L(n) asm volatile("s_waitcnt lgkmcnt(" #n ")" ::: "memory")
; template <class Epi, class Sched, bool ALIGN_EPI = false, bool SP2 = false>
; __device__ __forceinline__ void gemm_phase(PG8_LAS unsigned char* lds, const Gemm g, const Sched& S, const Epi& E, const int tid) {
;     ...
;             PG8_WAIT_V(8); PG8_WAIT_L(0); PG8_BAR; PG8_MMA(1, 0, At, B0); PG8_MMA(1, 1, At, B1); PG8_BAR; PG8_SCHED;
;             PG8_LDB(B0, 1, 0); PG8_LDB(B1, 1, 1); PG8_SCHED; PG8_LDA(At, 1, 0); PG8_STAGE(PG8_SA(0, 1), a2 + hstep, voffA);
;             PG8_WAIT_V(8); PG8_WAIT_L(0); PG8_BAR; PG8_MMA(0, 0, At, B0); PG8_MMA(0, 1, At, B1); PG8_BAR; PG8_SCHED;
	s_setprio 1
	s_waitcnt lgkmcnt(0)
	v_mfma_f32_16x16x32_bf16 v[62:65], v[164:167], v[198:201], 0
	v_mfma_f32_16x16x32_bf16 v[58:61], v[172:175], v[198:201], 0
	v_mfma_f32_16x16x32_bf16 v[54:57], v[164:167], v[206:209], 0
	v_mfma_f32_16x16x32_bf16 v[46:49], v[172:175], v[206:209], 0
	v_mfma_f32_16x16x32_bf16 v[38:41], v[164:167], v[214:217], 0
	v_mfma_f32_16x16x32_bf16 v[30:33], v[172:175], v[214:217], 0
	v_mfma_f32_16x16x32_bf16 v[22:25], v[164:167], v[222:225], 0
	v_mfma_f32_16x16x32_bf16 v[14:17], v[172:175], v[222:225], 0
	v_mfma_f32_16x16x32_bf16 v[62:65], v[168:171], v[202:205], v[62:65]
	v_mfma_f32_16x16x32_bf16 v[58:61], v[176:179], v[202:205], v[58:61]
	v_mfma_f32_16x16x32_bf16 v[54:57], v[168:171], v[210:213], v[54:57]
	v_mfma_f32_16x16x32_bf16 v[46:49], v[176:179], v[210:213], v[46:49]
	v_mfma_f32_16x16x32_bf16 v[38:41], v[168:171], v[218:221], v[38:41]
	v_mfma_f32_16x16x32_bf16 v[30:33], v[176:179], v[218:221], v[30:33]
	v_mfma_f32_16x16x32_bf16 v[22:25], v[168:171], v[226:229], v[22:25]
	v_mfma_f32_16x16x32_bf16 v[14:17], v[176:179], v[226:229], v[14:17]
	s_setprio 0
	s_setprio 1
	v_mfma_f32_16x16x32_bf16 v[50:53], v[180:183], v[198:201], 0
	v_mfma_f32_16x16x32_bf16 v[42:45], v[188:191], v[198:201], 0
	v_mfma_f32_16x16x32_bf16 v[34:37], v[180:183], v[206:209], 0
	v_mfma_f32_16x16x32_bf16 v[26:29], v[188:191], v[206:209], 0
	v_mfma_f32_16x16x32_bf16 v[18:21], v[180:183], v[214:217], 0
	v_mfma_f32_16x16x32_bf16 v[10:13], v[188:191], v[214:217], 0
	v_mfma_f32_16x16x32_bf16 v[6:9], v[180:183], v[222:225], 0
	v_mfma_f32_16x16x32_bf16 v[2:5], v[188:191], v[222:225], 0
	v_mfma_f32_16x16x32_bf16 v[50:53], v[184:187], v[202:205], v[50:53]
	v_mfma_f32_16x16x32_bf16 v[42:45], v[192:195], v[202:205], v[42:45]
	v_mfma_f32_16x16x32_bf16 v[34:37], v[184:187], v[210:213], v[34:37]
	v_mfma_f32_16x16x32_bf16 v[26:29], v[192:195], v[210:213], v[26:29]
	v_mfma_f32_16x16x32_bf16 v[18:21], v[184:187], v[218:221], v[18:21]
	v_mfma_f32_16x16x32_bf16 v[10:13], v[192:195], v[218:221], v[10:13]
	v_mfma_f32_16x16x32_bf16 v[6:9], v[184:187], v[226:229], v[6:9]
	v_mfma_f32_16x16x32_bf16 v[2:5], v[192:195], v[226:229], v[2:5]
	s_setprio 0
	s_barrier
	s_add_i32 s15, 0, 0x18000
	v_add_u32_e32 v131, s15, v152
	s_add_i32 s16, 0, 0x1c000
	ds_read_b128 v[164:167], v131
	ds_read_b128 v[168:171], v131 offset:1024
	ds_read_b128 v[172:175], v131 offset:2048
	ds_read_b128 v[176:179], v131 offset:3072
	v_add_u32_e32 v131, s16, v152
	ds_read_b128 v[180:183], v131
	ds_read_b128 v[184:187], v131 offset:1024
	ds_read_b128 v[188:191], v131 offset:2048
	ds_read_b128 v[192:195], v131 offset:3072
	s_add_u32 s18, s68, 0x80000
	s_addc_u32 s19, s69, 0
	s_mov_b32 m0, s44
	v_lshl_add_u64 v[244:245], s[18:19], 0, v[134:135]
	ds_read_b128 v[198:201], v163 offset:32768
	ds_read_b128 v[202:205], v163 offset:33792
	ds_read_b128 v[206:209], v163 offset:34816
	ds_read_b128 v[210:213], v163 offset:35840
	ds_read_b128 v[214:217], v163 offset:36864
	ds_read_b128 v[218:221], v163 offset:37888
	ds_read_b128 v[222:225], v163 offset:38912
	ds_read_b128 v[226:229], v163 offset:39936
	global_load_lds_dwordx4 v[244:245], off
	v_lshl_add_u64 v[244:245], s[18:19], 0, v[138:139]
	s_mov_b32 m0, s45
	s_nop 0
	global_load_lds_dwordx4 v[244:245], off
	s_waitcnt vmcnt(8)
	s_waitcnt lgkmcnt(0)
	s_barrier
	s_setprio 1
	s_waitcnt lgkmcnt(0)
	v_mfma_f32_16x16x32_bf16 v[126:129], v[164:167], v[198:201], v[126:129]
	v_mfma_f32_16x16x32_bf16 v[122:125], v[172:175], v[198:201], v[122:125]
	v_mfma_f32_16x16x32_bf16 v[118:121], v[164:167], v[206:209], v[118:121]
	v_mfma_f32_16x16x32_bf16 v[110:113], v[172:175], v[206:209], v[110:113]
	v_mfma_f32_16x16x32_bf16 v[102:105], v[164:167], v[214:217], v[102:105]
	v_mfma_f32_16x16x32_bf16 v[94:97], v[172:175], v[214:217], v[94:97]
	v_mfma_f32_16x16x32_bf16 v[86:89], v[164:167], v[222:225], v[86:89]
	v_mfma_f32_16x16x32_bf16 v[78:81], v[172:175], v[222:225], v[78:81]
	v_mfma_f32_16x16x32_bf16 v[126:129], v[168:171], v[202:205], v[126:129]
	v_mfma_f32_16x16x32_bf16 v[122:125], v[176:179], v[202:205], v[122:125]
	v_mfma_f32_16x16x32_bf16 v[118:121], v[168:171], v[210:213], v[118:121]
	v_mfma_f32_16x16x32_bf16 v[110:113], v[176:179], v[210:213], v[110:113]
	v_mfma_f32_16x16x32_bf16 v[102:105], v[168:171], v[218:221], v[102:105]
	v_mfma_f32_16x16x32_bf16 v[94:97], v[176:179], v[218:221], v[94:97]
	v_mfma_f32_16x16x32_bf16 v[86:89], v[168:171], v[226:229], v[86:89]
	v_mfma_f32_16x16x32_bf16 v[78:81], v[176:179], v[226:229], v[78:81]
	s_setprio 0
	s_setprio 1
	v_mfma_f32_16x16x32_bf16 v[114:117], v[180:183], v[198:201], v[114:117]
	v_mfma_f32_16x16x32_bf16 v[106:109], v[188:191], v[198:201], v[106:109]
	v_mfma_f32_16x16x32_bf16 v[98:101], v[180:183], v[206:209], v[98:101]
	v_mfma_f32_16x16x32_bf16 v[90:93], v[188:191], v[206:209], v[90:93]
	v_mfma_f32_16x16x32_bf16 v[82:85], v[180:183], v[214:217], v[82:85]
	v_mfma_f32_16x16x32_bf16 v[74:77], v[188:191], v[214:217], v[74:77]
	v_mfma_f32_16x16x32_bf16 v[70:73], v[180:183], v[222:225], v[70:73]
	v_mfma_f32_16x16x32_bf16 v[66:69], v[188:191], v[222:225], v[66:69]
	v_mfma_f32_16x16x32_bf16 v[114:117], v[184:187], v[202:205], v[114:117]
	v_mfma_f32_16x16x32_bf16 v[106:109], v[192:195], v[202:205], v[106:109]
	v_mfma_f32_16x16x32_bf16 v[98:101], v[184:187], v[210:213], v[98:101]
	v_mfma_f32_16x16x32_bf16 v[90:93], v[192:195], v[210:213], v[90:93]
	v_mfma_f32_16x16x32_bf16 v[82:85], v[184:187], v[218:221], v[82:85]
	v_mfma_f32_16x16x32_bf16 v[74:77], v[192:195], v[218:221], v[74:77]
	v_mfma_f32_16x16x32_bf16 v[70:73], v[184:187], v[226:229], v[70:73]
	v_mfma_f32_16x16x32_bf16 v[66:69], v[192:195], v[226:229], v[66:69]
	s_setprio 0
	s_barrier
; #define PG8_STAGE(bufoff, gbase, voff) do { _Pragma("unroll") for (int _i = 0; _i < 2; ++_i) \
;         __builtin_amdgcn_global_load_lds((const unsigned*)((const char*)(gbase) + (voff)[_i]), (PG8_LAS unsigned*)(lds + (bufoff) + ldsw + _i * 8192), 16, 0, 0); } while (0)
; #define PG8_LDA(dst, b, h) do { _Pragma("unroll") for (int m = 0; m < 4; ++m) _Pragma("unroll") for (int k = 0; k < 2; ++k) dst[m][k] = *(const PG8_LAS bf16x8*)(lds + PG8_SA(b, h) + aoff + m * 2048 + k * 1024); } while (0)
; #define PG8_MMA(ai, bj, At, Bt) do { __builtin_amdgcn_s_setprio(1); _Pragma("unroll") for (int m = 0; m < 4; ++m) _Pragma("unroll") for (int n = 0; n < 2; ++n) _Pragma("unroll") for (int k = 0; k < 2; ++k) \
;         acc[ai][bj][m][n] = __builtin_amdgcn_mfma_f32_16x16x32_bf16(Bt[n][k], At[m][k], acc[ai][bj][m][n], 0, 0, 0); __builtin_amdgcn_s_setprio(0); } while (0)
; #define PG8_WAIT_V(n) asm volatile("s_waitcnt vmcnt(" #n ")" ::: "memory")
; #define PG8_WAIT_L(n) asm volatile("s_waitcnt lgkmcnt(" #n ")" ::: "memory")
; #define PG8_BAR __builtin_amdgcn_s_barrier()
; #define PG8_SCHED __builtin_amdgcn_sched_barrier(0)
; #define PG8_STAGE(bufoff, gbase, voff) do { _Pragma("unroll") for (int _i = 0; _i < 2; ++_i) \
;         __builtin_amdgcn_global_load_lds((const unsigned*)((const char*)(gbase) + (voff)[_i]), (PG8_LAS unsigned*)(lds + (bufoff) + ldsw + _i * 8192), 16, 0, 0); } while (0)
; #define PG8_LDA(dst, b, h) do { _Pragma("unroll") for (int mb = 0; mb < 2; ++mb) _Pragma("unroll") for (int s = 0; s < 2; ++s) \
;         dst[mb][s] = cat8(*(const PG8_LAS bf16x8*)(lds + PG8_SA(b, h) + aoffk[s][0] + mb * 4096), *(const PG8_LAS bf16x8*)(lds + PG8_SA(b, h) + aoffk[s][1] + mb * 4096)); } while (0)
; #define PG8_WAIT_V(n) asm volatile("s_waitcnt vmcnt(" #n ")" ::: "memory")
; template <class Epi, class Sched, bool ALIGN_EPI = false, bool SP2 = false>
; __device__ __forceinline__ void gemm_phase(PG8_LAS unsigned char* lds, const Gemm g, const Sched& S, const Epi& E, const int tid) {
;     ...
;         for (int t = 0; t < nt; t += 2) {
;             const bool last = (t == nt - 2);
;     ...
;             PG8_LDA(At, 1, 1); PG8_STAGE(PG8_SB(1, 0), b3, voffB); PG8_STAGE(PG8_SB(1, 1), b3 + hstep, voffB); PG8_STAGE(PG8_SA(1, 0), a3, voffA);
;             PG8_WAIT_V(8); PG8_WAIT_L(0); PG8_BAR; PG8_MMA(1, 0, At, B0); PG8_MMA(1, 1, At, B1); PG8_BAR; PG8_SCHED;
	s_add_i32 s15, s15, s49
	v_lshl_add_u64 v[132:133], v[132:133], 0, s[34:35]
	s_mov_b32 m0, s15
	ds_read_b128 v[198:201], v163 offset:49152
	ds_read_b128 v[202:205], v163 offset:50176
	ds_read_b128 v[206:209], v163 offset:51200
	ds_read_b128 v[210:213], v163 offset:52224
	ds_read_b128 v[214:217], v163 offset:53248
	ds_read_b128 v[218:221], v163 offset:54272
	ds_read_b128 v[222:225], v163 offset:55296
	ds_read_b128 v[226:229], v163 offset:56320
	global_load_lds_dwordx4 v[132:133], off
	s_add_i32 m0, s15, 0x2000
	s_add_u32 s6, s6, 0x80080
	v_lshl_add_u64 v[132:133], v[148:149], 0, s[34:35]
	s_addc_u32 s7, s7, 0
	s_add_i32 s15, s16, s49
	global_load_lds_dwordx4 v[132:133], off
	v_lshl_add_u64 v[132:133], s[6:7], 0, v[136:137]
	s_mov_b32 m0, s15
	s_nop 0
	global_load_lds_dwordx4 v[132:133], off
	v_lshl_add_u64 v[132:133], s[6:7], 0, v[140:141]
	s_add_i32 m0, s15, 0x2000
	s_nop 0
	global_load_lds_dwordx4 v[132:133], off
	v_lshl_add_u64 v[132:133], v[230:231], 0, s[34:35]
	s_mov_b32 m0, s54
	s_nop 0
	global_load_lds_dwordx4 v[132:133], off
	v_lshl_add_u64 v[132:133], v[242:243], 0, s[34:35]
	s_mov_b32 m0, s55
	s_nop 0
	global_load_lds_dwordx4 v[132:133], off
	s_waitcnt vmcnt(8)
	s_waitcnt lgkmcnt(0)
	s_barrier
	s_setprio 1
	s_waitcnt lgkmcnt(0)
	v_mfma_f32_16x16x32_bf16 v[62:65], v[164:167], v[198:201], v[62:65]
	v_mfma_f32_16x16x32_bf16 v[58:61], v[172:175], v[198:201], v[58:61]
	v_mfma_f32_16x16x32_bf16 v[54:57], v[164:167], v[206:209], v[54:57]
	v_mfma_f32_16x16x32_bf16 v[46:49], v[172:175], v[206:209], v[46:49]
	v_mfma_f32_16x16x32_bf16 v[38:41], v[164:167], v[214:217], v[38:41]
	v_mfma_f32_16x16x32_bf16 v[30:33], v[172:175], v[214:217], v[30:33]
	v_mfma_f32_16x16x32_bf16 v[22:25], v[164:167], v[222:225], v[22:25]
	v_mfma_f32_16x16x32_bf16 v[14:17], v[172:175], v[222:225], v[14:17]
	v_mfma_f32_16x16x32_bf16 v[62:65], v[168:171], v[202:205], v[62:65]
	v_mfma_f32_16x16x32_bf16 v[58:61], v[176:179], v[202:205], v[58:61]
	v_mfma_f32_16x16x32_bf16 v[54:57], v[168:171], v[210:213], v[54:57]
	v_mfma_f32_16x16x32_bf16 v[46:49], v[176:179], v[210:213], v[46:49]
	v_mfma_f32_16x16x32_bf16 v[38:41], v[168:171], v[218:221], v[38:41]
	v_mfma_f32_16x16x32_bf16 v[30:33], v[176:179], v[218:221], v[30:33]
	v_mfma_f32_16x16x32_bf16 v[22:25], v[168:171], v[226:229], v[22:25]
	v_mfma_f32_16x16x32_bf16 v[14:17], v[176:179], v[226:229], v[14:17]
	s_setprio 0
	s_setprio 1
	v_mfma_f32_16x16x32_bf16 v[50:53], v[180:183], v[198:201], v[50:53]
	v_mfma_f32_16x16x32_bf16 v[42:45], v[188:191], v[198:201], v[42:45]
	v_mfma_f32_16x16x32_bf16 v[34:37], v[180:183], v[206:209], v[34:37]
	v_mfma_f32_16x16x32_bf16 v[26:29], v[188:191], v[206:209], v[26:29]
	v_mfma_f32_16x16x32_bf16 v[18:21], v[180:183], v[214:217], v[18:21]
	v_mfma_f32_16x16x32_bf16 v[10:13], v[188:191], v[214:217], v[10:13]
	v_mfma_f32_16x16x32_bf16 v[6:9], v[180:183], v[222:225], v[6:9]
	v_mfma_f32_16x16x32_bf16 v[2:5], v[188:191], v[222:225], v[2:5]
	v_mfma_f32_16x16x32_bf16 v[50:53], v[184:187], v[202:205], v[50:53]
	v_mfma_f32_16x16x32_bf16 v[42:45], v[192:195], v[202:205], v[42:45]
	v_mfma_f32_16x16x32_bf16 v[34:37], v[184:187], v[210:213], v[34:37]
	v_mfma_f32_16x16x32_bf16 v[26:29], v[192:195], v[210:213], v[26:29]
	v_mfma_f32_16x16x32_bf16 v[18:21], v[184:187], v[218:221], v[18:21]
	v_mfma_f32_16x16x32_bf16 v[10:13], v[192:195], v[218:221], v[10:13]
	v_mfma_f32_16x16x32_bf16 v[6:9], v[184:187], v[226:229], v[6:9]
	v_mfma_f32_16x16x32_bf16 v[2:5], v[192:195], v[226:229], v[2:5]
	s_setprio 0
	s_barrier
	s_add_i32 s13, s13, 2
	s_add_u32 s40, s40, 0x100
	s_addc_u32 s41, s41, 0
	s_add_u32 s11, s11, 0x100
	s_addc_u32 s12, s12, 0
	s_cmp_gt_u32 s13, 29
	s_cbranch_scc1 .Lpeel_exit_757

; #define PG8_BAR __builtin_amdgcn_s_barrier()
; #define PG8_BAR __builtin_amdgcn_s_barrier()
; template <class Epi, class Sched, bool ALIGN_EPI = false, bool SP2 = false>
; __device__ __forceinline__ void gemm_phase(PG8_LAS unsigned char* lds, const Gemm g, const Sched& S, const Epi& E, const int tid) {
;     ...
;         if constexpr (ALIGN_EPI) { if (wr == 0) PG8_BAR; }
.Lpeel_exit_757:
	s_and_b64 vcc, exec, s[70:71]
	s_cbranch_vccz .LBB0_760
	s_barrier

; #define PG8_STAGE(bufoff, gbase, voff) do { _Pragma("unroll") for (int _i = 0; _i < 2; ++_i) \
;         __builtin_amdgcn_global_load_lds((const unsigned*)((const char*)(gbase) + (voff)[_i]), (PG8_LAS unsigned*)(lds + (bufoff) + ldsw + _i * 8192), 16, 0, 0); } while (0)
; #define PG8_LDA(dst, b, h) do { _Pragma("unroll") for (int m = 0; m < 4; ++m) _Pragma("unroll") for (int k = 0; k < 2; ++k) dst[m][k] = *(const PG8_LAS bf16x8*)(lds + PG8_SA(b, h) + aoff + m * 2048 + k * 1024); } while (0)
; #define PG8_LDB(dst, b, h) do { _Pragma("unroll") for (int n = 0; n < 2; ++n) _Pragma("unroll") for (int k = 0; k < 2; ++k) dst[n][k] = *(const PG8_LAS bf16x8*)(lds + PG8_SB(b, h) + boff + n * 2048 + k * 1024); } while (0)
; #define PG8_WAIT_V(n) asm volatile("s_waitcnt vmcnt(" #n ")" ::: "memory")
; #define PG8_WAIT_L(n) asm volatile("s_waitcnt lgkmcnt(" #n ")" ::: "memory")
; #define PG8_BAR __builtin_amdgcn_s_barrier()
; #define PG8_SCHED __builtin_amdgcn_sched_barrier(0)
; #define PG8_WAIT_V(n) asm volatile("s_waitcnt vmcnt(" #n ")" ::: "memory")
; template <class Epi, class Sched, bool ALIGN_EPI = false, bool SP2 = false>
; __device__ __forceinline__ void gemm_phase(PG8_LAS unsigned char* lds, const Gemm g, const Sched& S, const Epi& E, const int tid) {
;     ...
;         const bool has_next = S.next(ui + 1, nxt);
;         const char* nA = has_next ? (const char*)g.A + (size_t)nxt.pm * tstep + (size_t)nxt.k0 * 2 : cA; const char* nB = has_next ? (const char*)g.Bt + (size_t)nxt.pn * tstep + (size_t)nxt.k0 * 2 : cB;
;         for (int t = 0; t < nt; t += 2) {
;             const bool last = (t == nt - 2);
;             const char* a1 = cA + (size_t)(t + 1) * kstep;
;             const char* a2 = last ? nA : cA + (size_t)(t + 2) * kstep; const char* b2 = last ? nB : cB + (size_t)(t + 2) * kstep;
;             const char* a3 = a2 + kstep; const char* b3 = b2 + kstep;
;             if (last && has_next) S.a_ready(nxt);
;             if constexpr (SP2) {
;             PG8_LDB(B0, 0, 0); PG8_LDB(B1, 0, 1); PG8_SCHED; PG8_LDA(At, 0, 0); PG8_STAGE(PG8_SA(1, 1), a1 + hstep, voffA);
;             PG8_WAIT_V(8); PG8_WAIT_L(0); PG8_BAR; PG8_MMA(0, 0, At, B0); PG8_MMA(0, 1, At, B1); PG8_BAR; PG8_SCHED;
;             PG8_LDA(At, 0, 1); PG8_STAGE(PG8_SB(0, 0), b2, voffB); PG8_STAGE(PG8_SB(0, 1), b2 + hstep, voffB); PG8_STAGE(PG8_SA(0, 0), a2, voffA);
.LBB0_1588:
	s_ashr_i32 s23, s22, 31
	s_lshl_b64 s[12:13], s[22:23], 20
	s_add_u32 s12, s33, s12
	s_addc_u32 s13, s19, s13
	s_ashr_i32 s17, s16, 31
	s_lshl_b64 s[42:43], s[16:17], 1
	s_add_u32 s40, s12, s42
	s_addc_u32 s41, s13, s43
	s_and_b64 s[12:13], s[28:29], exec
	s_cselect_b32 s12, s41, s47
	s_cselect_b32 s13, s40, s46
	s_ashr_i32 s21, s20, 31
	s_lshl_b64 s[48:49], s[20:21], 20
	s_add_u32 s17, s24, s48
	s_addc_u32 s21, s27, s49
	s_add_u32 s42, s17, s42
	s_addc_u32 s43, s21, s43
	s_and_b64 s[48:49], s[28:29], exec
	s_cselect_b32 s17, s43, s7
	s_cselect_b32 s21, s42, s6
	s_add_i32 s23, s64, -2
	s_add_u32 s46, s46, 0x80080
	s_addc_u32 s47, s47, 0
	s_add_u32 s39, s6, 0x100
	v_mov_b32_e32 v2, 0
	s_addc_u32 s45, s7, 0
	s_mov_b32 s6, 0
	s_add_i32 s63, s6, 2
	s_add_u32 s7, s46, 0xfff80080
	s_addc_u32 s48, s47, -1
	s_add_i32 s65, 0, 0x10000
	s_cmp_eq_u32 s23, s6
	s_cselect_b32 s49, s12, s48
	s_cselect_b32 s48, s13, s7
	s_cselect_b32 s7, s17, s45
	s_cselect_b32 s6, s21, s39
	s_add_i32 s68, 0, 0x14000
	v_add_u32_e32 v144, s65, v180
	v_add_u32_e32 v160, s68, v180
	ds_read_b128 v[132:135], v144
	ds_read_b128 v[136:139], v144 offset:1024
	ds_read_b128 v[140:143], v144 offset:2048
	ds_read_b128 v[144:147], v144 offset:3072
	ds_read_b128 v[148:151], v160
	ds_read_b128 v[152:155], v160 offset:1024
	ds_read_b128 v[156:159], v160 offset:2048
	ds_read_b128 v[160:163], v160 offset:3072
	v_lshl_add_u64 v[194:195], s[46:47], 0, v[172:173]
	s_add_i32 m0, s18, 0xc000
	ds_read_b128 v[176:179], v189
	ds_read_b128 v[190:193], v189 offset:1024
	ds_read_b128 v[198:201], v189 offset:2048
	ds_read_b128 v[202:205], v189 offset:3072
	ds_read_b128 v[206:209], v189 offset:4096
	ds_read_b128 v[210:213], v189 offset:5120
	ds_read_b128 v[214:217], v189 offset:6144
	ds_read_b128 v[218:221], v189 offset:7168
	global_load_lds_dwordx4 v[194:195], off
	v_lshl_add_u64 v[194:195], s[46:47], 0, v[174:175]
	s_add_i32 m0, s18, 0xe000
	s_nop 0
	global_load_lds_dwordx4 v[194:195], off
	s_waitcnt vmcnt(8)
	s_waitcnt lgkmcnt(0)
	s_barrier
	s_setprio 1
	s_waitcnt lgkmcnt(0)
	v_mfma_f32_16x16x32_bf16 v[126:129], v[132:135], v[176:179], 0
	v_mfma_f32_16x16x32_bf16 v[122:125], v[140:143], v[176:179], 0
	v_mfma_f32_16x16x32_bf16 v[114:117], v[132:135], v[198:201], 0
	v_mfma_f32_16x16x32_bf16 v[106:109], v[140:143], v[198:201], 0
	v_mfma_f32_16x16x32_bf16 v[98:101], v[132:135], v[206:209], 0
	v_mfma_f32_16x16x32_bf16 v[90:93], v[140:143], v[206:209], 0
	v_mfma_f32_16x16x32_bf16 v[82:85], v[132:135], v[214:217], 0
	v_mfma_f32_16x16x32_bf16 v[74:77], v[140:143], v[214:217], 0
	v_mfma_f32_16x16x32_bf16 v[126:129], v[136:139], v[190:193], v[126:129]
	v_mfma_f32_16x16x32_bf16 v[122:125], v[144:147], v[190:193], v[122:125]
	v_mfma_f32_16x16x32_bf16 v[114:117], v[136:139], v[202:205], v[114:117]
	v_mfma_f32_16x16x32_bf16 v[106:109], v[144:147], v[202:205], v[106:109]
	v_mfma_f32_16x16x32_bf16 v[98:101], v[136:139], v[210:213], v[98:101]
	v_mfma_f32_16x16x32_bf16 v[90:93], v[144:147], v[210:213], v[90:93]
	v_mfma_f32_16x16x32_bf16 v[82:85], v[136:139], v[218:221], v[82:85]
	v_mfma_f32_16x16x32_bf16 v[74:77], v[144:147], v[218:221], v[74:77]
	s_setprio 0
	s_setprio 1
	v_mfma_f32_16x16x32_bf16 v[118:121], v[148:151], v[176:179], 0
	v_mfma_f32_16x16x32_bf16 v[110:113], v[156:159], v[176:179], 0
	v_mfma_f32_16x16x32_bf16 v[102:105], v[148:151], v[198:201], 0
	v_mfma_f32_16x16x32_bf16 v[94:97], v[156:159], v[198:201], 0
	v_mfma_f32_16x16x32_bf16 v[86:89], v[148:151], v[206:209], 0
	v_mfma_f32_16x16x32_bf16 v[78:81], v[156:159], v[206:209], 0
	v_mfma_f32_16x16x32_bf16 v[70:73], v[148:151], v[214:217], 0
	v_mfma_f32_16x16x32_bf16 v[66:69], v[156:159], v[214:217], 0
	v_mfma_f32_16x16x32_bf16 v[118:121], v[152:155], v[190:193], v[118:121]
	v_mfma_f32_16x16x32_bf16 v[110:113], v[160:163], v[190:193], v[110:113]
	v_mfma_f32_16x16x32_bf16 v[102:105], v[152:155], v[202:205], v[102:105]
	v_mfma_f32_16x16x32_bf16 v[94:97], v[160:163], v[202:205], v[94:97]
	v_mfma_f32_16x16x32_bf16 v[86:89], v[152:155], v[210:213], v[86:89]
	v_mfma_f32_16x16x32_bf16 v[78:81], v[160:163], v[210:213], v[78:81]
	v_mfma_f32_16x16x32_bf16 v[70:73], v[152:155], v[218:221], v[70:73]
	v_mfma_f32_16x16x32_bf16 v[66:69], v[160:163], v[218:221], v[66:69]
	s_setprio 0
	s_barrier
	s_add_i32 s65, s65, s36
	v_lshl_add_u64 v[194:195], s[6:7], 0, v[166:167]
	s_mov_b32 m0, s65
	ds_read_b128 v[176:179], v189 offset:16384
	ds_read_b128 v[190:193], v189 offset:17408
	ds_read_b128 v[198:201], v189 offset:18432
	ds_read_b128 v[202:205], v189 offset:19456
	ds_read_b128 v[206:209], v189 offset:20480
	ds_read_b128 v[210:213], v189 offset:21504
	ds_read_b128 v[214:217], v189 offset:22528
	ds_read_b128 v[218:221], v189 offset:23552
	global_load_lds_dwordx4 v[194:195], off
	s_add_i32 m0, s65, 0x2000
	s_add_u32 s66, s6, 0x80000
	v_lshl_add_u64 v[222:223], s[6:7], 0, v[170:171]
	s_addc_u32 s67, s7, 0
	s_add_i32 s65, s68, s36
	global_load_lds_dwordx4 v[222:223], off
	v_lshl_add_u64 v[224:225], s[66:67], 0, v[166:167]
	s_mov_b32 m0, s65
	v_lshl_add_u64 v[226:227], s[48:49], 0, v[168:169]
	global_load_lds_dwordx4 v[224:225], off
	v_lshl_add_u64 v[224:225], s[66:67], 0, v[170:171]
	s_add_i32 m0, s65, 0x2000
	s_nop 0
	global_load_lds_dwordx4 v[224:225], off
	v_lshl_add_u64 v[224:225], s[48:49], 0, v[164:165]
	s_mov_b32 m0, s18
	s_nop 0
	global_load_lds_dwordx4 v[224:225], off
	s_mov_b32 m0, s31
	s_nop 0
	global_load_lds_dwordx4 v[226:227], off
	s_waitcnt vmcnt(8)
	s_waitcnt lgkmcnt(0)
	s_barrier
; #define PG8_STAGE(bufoff, gbase, voff) do { _Pragma("unroll") for (int _i = 0; _i < 2; ++_i) \
;         __builtin_amdgcn_global_load_lds((const unsigned*)((const char*)(gbase) + (voff)[_i]), (PG8_LAS unsigned*)(lds + (bufoff) + ldsw + _i * 8192), 16, 0, 0); } while (0)
; #define PG8_LDA(dst, b, h) do { _Pragma("unroll") for (int m = 0; m < 4; ++m) _Pragma("unroll") for (int k = 0; k < 2; ++k) dst[m][k] = *(const PG8_LAS bf16x8*)(lds + PG8_SA(b, h) + aoff + m * 2048 + k * 1024); } while (0)
; #define PG8_LDB(dst, b, h) do { _Pragma("unroll") for (int n = 0; n < 2; ++n) _Pragma("unroll") for (int k = 0; k < 2; ++k) dst[n][k] = *(const PG8_LAS bf16x8*)(lds + PG8_SB(b, h) + boff + n * 2048 + k * 1024); } while (0)
; #define PG8_MMA(ai, bj, At, Bt) do { __builtin_amdgcn_s_setprio(1); _Pragma("unroll") for (int m = 0; m < 4; ++m) _Pragma("unroll") for (int n = 0; n < 2; ++n) _Pragma("unroll") for (int k = 0; k < 2; ++k) \
;         acc[ai][bj][m][n] = __builtin_amdgcn_mfma_f32_16x16x32_bf16(Bt[n][k], At[m][k], acc[ai][bj][m][n], 0, 0, 0); __builtin_amdgcn_s_setprio(0); } while (0)
; #define PG8_WAIT_V(n) asm volatile("s_waitcnt vmcnt(" #n ")" ::: "memory")
; #define PG8_WAIT_L(n) asm volatile("s_waitcnt lgkmcnt(" #n ")" ::: "memory")
; #define PG8_BAR __builtin_amdgcn_s_barrier()
; #define PG8_SCHED __builtin_amdgcn_sched_barrier(0)
; #define PG8_STAGE(bufoff, gbase, voff) do { _Pragma("unroll") for (int _i = 0; _i < 2; ++_i) \
;         __builtin_amdgcn_global_load_lds((const unsigned*)((const char*)(gbase) + (voff)[_i]), (PG8_LAS unsigned*)(lds + (bufoff) + ldsw + _i * 8192), 16, 0, 0); } while (0)
; #define PG8_WAIT_V(n) asm volatile("s_waitcnt vmcnt(" #n ")" ::: "memory")
; #define PG8_WAIT_L(n) asm volatile("s_waitcnt lgkmcnt(" #n ")" ::: "memory")
; template <class Epi, class Sched, bool ALIGN_EPI = false, bool SP2 = false>
; __device__ __forceinline__ void gemm_phase(PG8_LAS unsigned char* lds, const Gemm g, const Sched& S, const Epi& E, const int tid) {
;     ...
;             PG8_WAIT_V(8); PG8_WAIT_L(0); PG8_BAR; PG8_MMA(1, 0, At, B0); PG8_MMA(1, 1, At, B1); PG8_BAR; PG8_SCHED;
;             PG8_LDB(B0, 1, 0); PG8_LDB(B1, 1, 1); PG8_SCHED; PG8_LDA(At, 1, 0); PG8_STAGE(PG8_SA(0, 1), a2 + hstep, voffA);
;             PG8_WAIT_V(8); PG8_WAIT_L(0); PG8_BAR; PG8_MMA(0, 0, At, B0); PG8_MMA(0, 1, At, B1); PG8_BAR; PG8_SCHED;
	s_setprio 1
	s_waitcnt lgkmcnt(0)
	v_mfma_f32_16x16x32_bf16 v[62:65], v[132:135], v[176:179], 0
	v_mfma_f32_16x16x32_bf16 v[58:61], v[140:143], v[176:179], 0
	v_mfma_f32_16x16x32_bf16 v[50:53], v[132:135], v[198:201], 0
	v_mfma_f32_16x16x32_bf16 v[42:45], v[140:143], v[198:201], 0
	v_mfma_f32_16x16x32_bf16 v[34:37], v[132:135], v[206:209], 0
	v_mfma_f32_16x16x32_bf16 v[26:29], v[140:143], v[206:209], 0
	v_mfma_f32_16x16x32_bf16 v[18:21], v[132:135], v[214:217], 0
	v_mfma_f32_16x16x32_bf16 v[10:13], v[140:143], v[214:217], 0
	v_mfma_f32_16x16x32_bf16 v[62:65], v[136:139], v[190:193], v[62:65]
	v_mfma_f32_16x16x32_bf16 v[58:61], v[144:147], v[190:193], v[58:61]
	v_mfma_f32_16x16x32_bf16 v[50:53], v[136:139], v[202:205], v[50:53]
	v_mfma_f32_16x16x32_bf16 v[42:45], v[144:147], v[202:205], v[42:45]
	v_mfma_f32_16x16x32_bf16 v[34:37], v[136:139], v[210:213], v[34:37]
	v_mfma_f32_16x16x32_bf16 v[26:29], v[144:147], v[210:213], v[26:29]
	v_mfma_f32_16x16x32_bf16 v[18:21], v[136:139], v[218:221], v[18:21]
	v_mfma_f32_16x16x32_bf16 v[10:13], v[144:147], v[218:221], v[10:13]
	s_setprio 0
	s_setprio 1
	v_mfma_f32_16x16x32_bf16 v[54:57], v[148:151], v[176:179], 0
	v_mfma_f32_16x16x32_bf16 v[46:49], v[156:159], v[176:179], 0
	v_mfma_f32_16x16x32_bf16 v[38:41], v[148:151], v[198:201], 0
	v_mfma_f32_16x16x32_bf16 v[30:33], v[156:159], v[198:201], 0
	v_mfma_f32_16x16x32_bf16 v[22:25], v[148:151], v[206:209], 0
	v_mfma_f32_16x16x32_bf16 v[14:17], v[156:159], v[206:209], 0
	v_mfma_f32_16x16x32_bf16 v[6:9], v[148:151], v[214:217], 0
	v_mfma_f32_16x16x32_bf16 v[2:5], v[156:159], v[214:217], 0
	v_mfma_f32_16x16x32_bf16 v[54:57], v[152:155], v[190:193], v[54:57]
	v_mfma_f32_16x16x32_bf16 v[46:49], v[160:163], v[190:193], v[46:49]
	v_mfma_f32_16x16x32_bf16 v[38:41], v[152:155], v[202:205], v[38:41]
	v_mfma_f32_16x16x32_bf16 v[30:33], v[160:163], v[202:205], v[30:33]
	v_mfma_f32_16x16x32_bf16 v[22:25], v[152:155], v[210:213], v[22:25]
	v_mfma_f32_16x16x32_bf16 v[14:17], v[160:163], v[210:213], v[14:17]
	v_mfma_f32_16x16x32_bf16 v[6:9], v[152:155], v[218:221], v[6:9]
	v_mfma_f32_16x16x32_bf16 v[2:5], v[160:163], v[218:221], v[2:5]
	s_setprio 0
	s_barrier
	s_add_i32 s65, 0, 0x18000
	s_add_i32 s66, 0, 0x1c000
	v_add_u32_e32 v144, s65, v180
	v_add_u32_e32 v160, s66, v180
	ds_read_b128 v[132:135], v144
	ds_read_b128 v[136:139], v144 offset:1024
	ds_read_b128 v[140:143], v144 offset:2048
	ds_read_b128 v[144:147], v144 offset:3072
	ds_read_b128 v[148:151], v160
	ds_read_b128 v[152:155], v160 offset:1024
	ds_read_b128 v[156:159], v160 offset:2048
	ds_read_b128 v[160:163], v160 offset:3072
	s_add_u32 s48, s48, 0x80000
	s_addc_u32 s49, s49, 0
	s_mov_b32 m0, s37
	v_lshl_add_u64 v[228:229], s[48:49], 0, v[164:165]
	ds_read_b128 v[176:179], v189 offset:32768
	ds_read_b128 v[190:193], v189 offset:33792
	ds_read_b128 v[198:201], v189 offset:34816
	ds_read_b128 v[202:205], v189 offset:35840
	ds_read_b128 v[206:209], v189 offset:36864
	ds_read_b128 v[210:213], v189 offset:37888
	ds_read_b128 v[214:217], v189 offset:38912
	ds_read_b128 v[218:221], v189 offset:39936
	global_load_lds_dwordx4 v[228:229], off
	v_lshl_add_u64 v[228:229], s[48:49], 0, v[168:169]
	s_mov_b32 m0, s50
	s_nop 0
	global_load_lds_dwordx4 v[228:229], off
	s_waitcnt vmcnt(8)
	s_waitcnt lgkmcnt(0)
	s_barrier
	s_setprio 1
	s_waitcnt lgkmcnt(0)
	v_mfma_f32_16x16x32_bf16 v[126:129], v[132:135], v[176:179], v[126:129]
	v_mfma_f32_16x16x32_bf16 v[122:125], v[140:143], v[176:179], v[122:125]
	v_mfma_f32_16x16x32_bf16 v[114:117], v[132:135], v[198:201], v[114:117]
	v_mfma_f32_16x16x32_bf16 v[106:109], v[140:143], v[198:201], v[106:109]
	v_mfma_f32_16x16x32_bf16 v[98:101], v[132:135], v[206:209], v[98:101]
	v_mfma_f32_16x16x32_bf16 v[90:93], v[140:143], v[206:209], v[90:93]
	v_mfma_f32_16x16x32_bf16 v[82:85], v[132:135], v[214:217], v[82:85]
	v_mfma_f32_16x16x32_bf16 v[74:77], v[140:143], v[214:217], v[74:77]
	v_mfma_f32_16x16x32_bf16 v[126:129], v[136:139], v[190:193], v[126:129]
	v_mfma_f32_16x16x32_bf16 v[122:125], v[144:147], v[190:193], v[122:125]
	v_mfma_f32_16x16x32_bf16 v[114:117], v[136:139], v[202:205], v[114:117]
	v_mfma_f32_16x16x32_bf16 v[106:109], v[144:147], v[202:205], v[106:109]
	v_mfma_f32_16x16x32_bf16 v[98:101], v[136:139], v[210:213], v[98:101]
	v_mfma_f32_16x16x32_bf16 v[90:93], v[144:147], v[210:213], v[90:93]
	v_mfma_f32_16x16x32_bf16 v[82:85], v[136:139], v[218:221], v[82:85]
	v_mfma_f32_16x16x32_bf16 v[74:77], v[144:147], v[218:221], v[74:77]
	s_setprio 0
	s_setprio 1
	v_mfma_f32_16x16x32_bf16 v[118:121], v[148:151], v[176:179], v[118:121]
	v_mfma_f32_16x16x32_bf16 v[110:113], v[156:159], v[176:179], v[110:113]
	v_mfma_f32_16x16x32_bf16 v[102:105], v[148:151], v[198:201], v[102:105]
	v_mfma_f32_16x16x32_bf16 v[94:97], v[156:159], v[198:201], v[94:97]
	v_mfma_f32_16x16x32_bf16 v[86:89], v[148:151], v[206:209], v[86:89]
	v_mfma_f32_16x16x32_bf16 v[78:81], v[156:159], v[206:209], v[78:81]
	v_mfma_f32_16x16x32_bf16 v[70:73], v[148:151], v[214:217], v[70:73]
	v_mfma_f32_16x16x32_bf16 v[66:69], v[156:159], v[214:217], v[66:69]
	v_mfma_f32_16x16x32_bf16 v[118:121], v[152:155], v[190:193], v[118:121]
	v_mfma_f32_16x16x32_bf16 v[110:113], v[160:163], v[190:193], v[110:113]
	v_mfma_f32_16x16x32_bf16 v[102:105], v[152:155], v[202:205], v[102:105]
	v_mfma_f32_16x16x32_bf16 v[94:97], v[160:163], v[202:205], v[94:97]
	v_mfma_f32_16x16x32_bf16 v[86:89], v[152:155], v[210:213], v[86:89]
	v_mfma_f32_16x16x32_bf16 v[78:81], v[160:163], v[210:213], v[78:81]
	v_mfma_f32_16x16x32_bf16 v[70:73], v[152:155], v[218:221], v[70:73]
	v_mfma_f32_16x16x32_bf16 v[66:69], v[160:163], v[218:221], v[66:69]
	s_setprio 0
	s_barrier
; #define PG8_STAGE(bufoff, gbase, voff) do { _Pragma("unroll") for (int _i = 0; _i < 2; ++_i) \
;         __builtin_amdgcn_global_load_lds((const unsigned*)((const char*)(gbase) + (voff)[_i]), (PG8_LAS unsigned*)(lds + (bufoff) + ldsw + _i * 8192), 16, 0, 0); } while (0)
; #define PG8_LDA(dst, b, h) do { _Pragma("unroll") for (int m = 0; m < 4; ++m) _Pragma("unroll") for (int k = 0; k < 2; ++k) dst[m][k] = *(const PG8_LAS bf16x8*)(lds + PG8_SA(b, h) + aoff + m * 2048 + k * 1024); } while (0)
; #define PG8_MMA(ai, bj, At, Bt) do { __builtin_amdgcn_s_setprio(1); _Pragma("unroll") for (int m = 0; m < 4; ++m) _Pragma("unroll") for (int n = 0; n < 2; ++n) _Pragma("unroll") for (int k = 0; k < 2; ++k) \
;         acc[ai][bj][m][n] = __builtin_amdgcn_mfma_f32_16x16x32_bf16(Bt[n][k], At[m][k], acc[ai][bj][m][n], 0, 0, 0); __builtin_amdgcn_s_setprio(0); } while (0)
; #define PG8_WAIT_V(n) asm volatile("s_waitcnt vmcnt(" #n ")" ::: "memory")
; #define PG8_WAIT_L(n) asm volatile("s_waitcnt lgkmcnt(" #n ")" ::: "memory")
; #define PG8_BAR __builtin_amdgcn_s_barrier()
; #define PG8_SCHED __builtin_amdgcn_sched_barrier(0)
; #define PG8_STAGE(bufoff, gbase, voff) do { _Pragma("unroll") for (int _i = 0; _i < 2; ++_i) \
;         __builtin_amdgcn_global_load_lds((const unsigned*)((const char*)(gbase) + (voff)[_i]), (PG8_LAS unsigned*)(lds + (bufoff) + ldsw + _i * 8192), 16, 0, 0); } while (0)
; #define PG8_LDA(dst, b, h) do { _Pragma("unroll") for (int mb = 0; mb < 2; ++mb) _Pragma("unroll") for (int s = 0; s < 2; ++s) \
;         dst[mb][s] = cat8(*(const PG8_LAS bf16x8*)(lds + PG8_SA(b, h) + aoffk[s][0] + mb * 4096), *(const PG8_LAS bf16x8*)(lds + PG8_SA(b, h) + aoffk[s][1] + mb * 4096)); } while (0)
; #define PG8_WAIT_V(n) asm volatile("s_waitcnt vmcnt(" #n ")" ::: "memory")
; template <class Epi, class Sched, bool ALIGN_EPI = false, bool SP2 = false>
; __device__ __forceinline__ void gemm_phase(PG8_LAS unsigned char* lds, const Gemm g, const Sched& S, const Epi& E, const int tid) {
;     ...
;         for (int t = 0; t < nt; t += 2) {
;             const bool last = (t == nt - 2);
;     ...
;             PG8_LDA(At, 1, 1); PG8_STAGE(PG8_SB(1, 0), b3, voffB); PG8_STAGE(PG8_SB(1, 1), b3 + hstep, voffB); PG8_STAGE(PG8_SA(1, 0), a3, voffA);
;             PG8_WAIT_V(8); PG8_WAIT_L(0); PG8_BAR; PG8_MMA(1, 0, At, B0); PG8_MMA(1, 1, At, B1); PG8_BAR; PG8_SCHED;
	s_add_i32 s48, s65, s36
	v_lshl_add_u64 v[194:195], v[194:195], 0, s[34:35]
	s_mov_b32 m0, s48
	ds_read_b128 v[176:179], v189 offset:49152
	ds_read_b128 v[190:193], v189 offset:50176
	ds_read_b128 v[198:201], v189 offset:51200
	ds_read_b128 v[202:205], v189 offset:52224
	ds_read_b128 v[206:209], v189 offset:53248
	ds_read_b128 v[210:213], v189 offset:54272
	ds_read_b128 v[214:217], v189 offset:55296
	ds_read_b128 v[218:221], v189 offset:56320
	global_load_lds_dwordx4 v[194:195], off
	s_add_i32 m0, s48, 0x2000
	s_add_u32 s6, s6, 0x80080
	v_lshl_add_u64 v[194:195], v[222:223], 0, s[34:35]
	s_addc_u32 s7, s7, 0
	s_add_i32 s48, s66, s36
	global_load_lds_dwordx4 v[194:195], off
	v_lshl_add_u64 v[194:195], s[6:7], 0, v[166:167]
	s_mov_b32 m0, s48
	s_nop 0
	global_load_lds_dwordx4 v[194:195], off
	v_lshl_add_u64 v[194:195], s[6:7], 0, v[170:171]
	s_add_i32 m0, s48, 0x2000
	s_nop 0
	global_load_lds_dwordx4 v[194:195], off
	v_lshl_add_u64 v[194:195], v[224:225], 0, s[34:35]
	s_mov_b32 m0, s26
	s_nop 0
	global_load_lds_dwordx4 v[194:195], off
	v_lshl_add_u64 v[194:195], v[226:227], 0, s[34:35]
	s_mov_b32 m0, s52
	s_nop 0
	global_load_lds_dwordx4 v[194:195], off
	s_waitcnt vmcnt(8)
	s_waitcnt lgkmcnt(0)
	s_barrier
	s_setprio 1
	s_waitcnt lgkmcnt(0)
	v_mfma_f32_16x16x32_bf16 v[62:65], v[132:135], v[176:179], v[62:65]
	v_mfma_f32_16x16x32_bf16 v[58:61], v[140:143], v[176:179], v[58:61]
	v_mfma_f32_16x16x32_bf16 v[50:53], v[132:135], v[198:201], v[50:53]
	v_mfma_f32_16x16x32_bf16 v[42:45], v[140:143], v[198:201], v[42:45]
	v_mfma_f32_16x16x32_bf16 v[34:37], v[132:135], v[206:209], v[34:37]
	v_mfma_f32_16x16x32_bf16 v[26:29], v[140:143], v[206:209], v[26:29]
	v_mfma_f32_16x16x32_bf16 v[18:21], v[132:135], v[214:217], v[18:21]
	v_mfma_f32_16x16x32_bf16 v[10:13], v[140:143], v[214:217], v[10:13]
	v_mfma_f32_16x16x32_bf16 v[62:65], v[136:139], v[190:193], v[62:65]
	v_mfma_f32_16x16x32_bf16 v[58:61], v[144:147], v[190:193], v[58:61]
	v_mfma_f32_16x16x32_bf16 v[50:53], v[136:139], v[202:205], v[50:53]
	v_mfma_f32_16x16x32_bf16 v[42:45], v[144:147], v[202:205], v[42:45]
	v_mfma_f32_16x16x32_bf16 v[34:37], v[136:139], v[210:213], v[34:37]
	v_mfma_f32_16x16x32_bf16 v[26:29], v[144:147], v[210:213], v[26:29]
	v_mfma_f32_16x16x32_bf16 v[18:21], v[136:139], v[218:221], v[18:21]
	v_mfma_f32_16x16x32_bf16 v[10:13], v[144:147], v[218:221], v[10:13]
	s_setprio 0
	s_setprio 1
	v_mfma_f32_16x16x32_bf16 v[54:57], v[148:151], v[176:179], v[54:57]
	v_mfma_f32_16x16x32_bf16 v[46:49], v[156:159], v[176:179], v[46:49]
	v_mfma_f32_16x16x32_bf16 v[38:41], v[148:151], v[198:201], v[38:41]
	v_mfma_f32_16x16x32_bf16 v[30:33], v[156:159], v[198:201], v[30:33]
	v_mfma_f32_16x16x32_bf16 v[22:25], v[148:151], v[206:209], v[22:25]
	v_mfma_f32_16x16x32_bf16 v[14:17], v[156:159], v[206:209], v[14:17]
	v_mfma_f32_16x16x32_bf16 v[6:9], v[148:151], v[214:217], v[6:9]
	v_mfma_f32_16x16x32_bf16 v[2:5], v[156:159], v[214:217], v[2:5]
	v_mfma_f32_16x16x32_bf16 v[54:57], v[152:155], v[190:193], v[54:57]
	v_mfma_f32_16x16x32_bf16 v[46:49], v[160:163], v[190:193], v[46:49]
	v_mfma_f32_16x16x32_bf16 v[38:41], v[152:155], v[202:205], v[38:41]
	v_mfma_f32_16x16x32_bf16 v[30:33], v[160:163], v[202:205], v[30:33]
	v_mfma_f32_16x16x32_bf16 v[22:25], v[152:155], v[210:213], v[22:25]
	v_mfma_f32_16x16x32_bf16 v[14:17], v[160:163], v[210:213], v[14:17]
	v_mfma_f32_16x16x32_bf16 v[6:9], v[152:155], v[218:221], v[6:9]
	v_mfma_f32_16x16x32_bf16 v[2:5], v[160:163], v[218:221], v[2:5]
	s_setprio 0
	s_barrier
	s_add_u32 s46, s46, 0x100
	s_addc_u32 s47, s47, 0
	s_add_u32 s39, s39, 0x100
	s_addc_u32 s45, s45, 0
	s_cmp_ge_i32 s63, s64
	s_mov_b32 s6, s63
	s_cbranch_scc1 .Lpeel_exit_1589

; #define PG8_BAR __builtin_amdgcn_s_barrier()
; #define PG8_BAR __builtin_amdgcn_s_barrier()
; template <class Epi, class Sched, bool ALIGN_EPI = false, bool SP2 = false>
; __device__ __forceinline__ void gemm_phase(PG8_LAS unsigned char* lds, const Gemm g, const Sched& S, const Epi& E, const int tid) {
;     ...
;         if constexpr (ALIGN_EPI) { if (wr == 0) PG8_BAR; }
.Lpeel_exit_1589:
	s_and_b64 vcc, exec, s[4:5]
	s_cbranch_vccz .LBB0_1592
	s_barrier

; #define PG8_STAGE(bufoff, gbase, voff) do { _Pragma("unroll") for (int _i = 0; _i < 2; ++_i) \
;         __builtin_amdgcn_global_load_lds((const unsigned*)((const char*)(gbase) + (voff)[_i]), (PG8_LAS unsigned*)(lds + (bufoff) + ldsw + _i * 8192), 16, 0, 0); } while (0)
; #define PG8_LDA(dst, b, h) do { _Pragma("unroll") for (int m = 0; m < 4; ++m) _Pragma("unroll") for (int k = 0; k < 2; ++k) dst[m][k] = *(const PG8_LAS bf16x8*)(lds + PG8_SA(b, h) + aoff + m * 2048 + k * 1024); } while (0)
; #define PG8_LDB(dst, b, h) do { _Pragma("unroll") for (int n = 0; n < 2; ++n) _Pragma("unroll") for (int k = 0; k < 2; ++k) dst[n][k] = *(const PG8_LAS bf16x8*)(lds + PG8_SB(b, h) + boff + n * 2048 + k * 1024); } while (0)
; #define PG8_WAIT_V(n) asm volatile("s_waitcnt vmcnt(" #n ")" ::: "memory")
; #define PG8_WAIT_L(n) asm volatile("s_waitcnt lgkmcnt(" #n ")" ::: "memory")
; #define PG8_BAR __builtin_amdgcn_s_barrier()
; #define PG8_SCHED __builtin_amdgcn_sched_barrier(0)
; template <class Epi, class Sched, int SCW, int SCX, int SCW1 = SCW>
; __device__ __forceinline__ void gemm_phase_f8(PG8_LAS unsigned char* lds, const Gemm g, const Sched& S, const Epi& E, const int tid) {
;     ...
;         const bool has_next = S.next(ui + 1, nxt);
;         const char* nA = has_next ? (const char*)g.A + (size_t)nxt.pm * tstep + (size_t)nxt.k0 : cA; const char* nB = has_next ? (const char*)g.Bt + (size_t)nxt.pn * tstep + (size_t)nxt.k0 * 256 : cB;
;         for (int t = 0; t < nt; t += 2) {
;             const bool last = (t == nt - 2);
;             const char* a1 = cA + (size_t)(t + 1) * kstep;
;             const char* a2 = last ? nA : cA + (size_t)(t + 2) * kstep; const char* b2 = last ? nB : cB + (size_t)(t + 2) * kstepB;
;             const char* a3 = a2 + kstep; const char* b3 = b2 + kstepB;
;             if (last && has_next) S.a_ready(nxt);
;             PG8_LDB(B0, 0, 0); PG8_LDB(B1, 0, 1); PG8_SCHED; PG8_LDA(At, 0, 0); PG8_STAGE(PG8_SA(1, 1), a1 + hstep, voffA);
;             PG8_WAIT_V(8); PG8_WAIT_L(0); PG8_BAR; PG8_MMA(0, 0, At, B0); PG8_MMA(0, 1, At, B1); PG8_BAR; PG8_SCHED;
;             PG8_LDA(At, 0, 1); PG8_STAGE(PG8_SB(0, 0), b2, voffB); PG8_STAGE(PG8_SB(0, 1), b2 + hstepB, voffB); PG8_STAGE(PG8_SA(0, 0), a2, voffA);
;             PG8_WAIT_V(8); PG8_WAIT_L(0); PG8_BAR; PG8_MMA(1, 0, At, B0); PG8_MMA(1, 1, At, B1); PG8_BAR; PG8_SCHED;
.LBB0_1895:
	s_ashr_i32 s15, s14, 31
	s_lshl_b64 s[22:23], s[14:15], 19
	s_add_u32 s15, s44, s22
	s_addc_u32 s21, s45, s23
	s_ashr_i32 s17, s16, 31
	s_add_u32 s22, s15, s16
	s_addc_u32 s23, s21, s17
	s_and_b64 s[28:29], s[10:11], exec
	s_cselect_b32 s15, s23, s41
	s_cselect_b32 s63, s22, s40
	s_ashr_i32 s21, s20, 31
	s_lshl_b64 s[28:29], s[20:21], 19
	s_add_u32 s21, s46, s28
	s_addc_u32 s42, s47, s29
	s_lshl_b64 s[28:29], s[16:17], 8
	s_add_u32 s28, s21, s28
	s_addc_u32 s29, s42, s29
	s_and_b64 s[42:43], s[10:11], exec
	s_cselect_b32 s17, s29, s7
	s_cselect_b32 s21, s28, s6
	s_add_u32 s64, s6, 0x10000
	s_addc_u32 s65, s7, 0
	s_add_u32 s40, s40, 0x40080
	v_mov_b32_e32 v18, 0
	s_addc_u32 s41, s41, 0
	s_mov_b32 s66, -2
	s_add_u32 s6, s40, 0xfffc0080
	s_addc_u32 s7, s41, -1
	s_add_i32 s67, 0, 0x10000
	s_cmp_eq_u32 s66, 12
	v_add_u32_e32 v144, s67, v131
	s_cselect_b32 s43, s15, s7
	s_cselect_b32 s42, s63, s6
	v_add_u32_e32 v145, s67, v150
	ds_read_b128 v[160:163], v144
	ds_read_b128 v[164:167], v145
	v_add_u32_e32 v144, s67, v151
	s_cselect_b32 s7, s17, s65
	s_cselect_b32 s6, s21, s64
	s_add_i32 s70, 0, 0x14000
	v_add_u32_e32 v145, s67, v152
	ds_read_b128 v[168:171], v144
	ds_read_b128 v[172:175], v145
	v_add_u32_e32 v144, s70, v131
	v_add_u32_e32 v145, s70, v150
	ds_read_b128 v[176:179], v144
	ds_read_b128 v[180:183], v145
	v_add_u32_e32 v144, s70, v151
	v_add_u32_e32 v145, s70, v152
	ds_read_b128 v[184:187], v144
	ds_read_b128 v[188:191], v145
	v_lshl_add_u64 v[144:145], s[40:41], 0, v[140:141]
	s_add_i32 m0, s31, 0xc000
	ds_read_b128 v[198:201], v155
	ds_read_b128 v[206:209], v155 offset:4096
	ds_read_b128 v[202:205], v156
	ds_read_b128 v[210:213], v156 offset:4096
	ds_read_b128 v[214:217], v157
	ds_read_b128 v[222:225], v157 offset:4096
	ds_read_b128 v[218:221], v158
	ds_read_b128 v[226:229], v158 offset:4096
	global_load_lds_dwordx4 v[144:145], off
	v_lshl_add_u64 v[144:145], s[40:41], 0, v[142:143]
	s_add_i32 m0, s31, 0xe000
	s_nop 0
	global_load_lds_dwordx4 v[144:145], off
	s_waitcnt vmcnt(8)
	s_waitcnt lgkmcnt(0)
	s_barrier
	s_setprio 1
	s_waitcnt lgkmcnt(0)
	v_mfma_scale_f32_32x32x64_f8f6f4 v[98:113], v[160:167], v[198:205], 0, v233, v232 op_sel_hi:[0,0,0]
	v_mfma_scale_f32_32x32x64_f8f6f4 v[66:81], v[160:167], v[206:213], 0, v233, v232 op_sel_hi:[0,0,0]
	v_mfma_scale_f32_32x32x64_f8f6f4 v[98:113], v[168:175], v[214:221], v[98:113], v233, v232 op_sel_hi:[0,0,0]
	v_mfma_scale_f32_32x32x64_f8f6f4 v[66:81], v[168:175], v[222:229], v[66:81], v233, v232 op_sel_hi:[0,0,0]
	s_setprio 0
	s_setprio 1
	v_mfma_scale_f32_32x32x64_f8f6f4 v[114:129], v[176:183], v[198:205], 0, v232, v232 op_sel_hi:[0,0,0]
	v_mfma_scale_f32_32x32x64_f8f6f4 v[82:97], v[176:183], v[206:213], 0, v232, v232 op_sel_hi:[0,0,0]
	v_mfma_scale_f32_32x32x64_f8f6f4 v[114:129], v[184:191], v[214:221], v[114:129], v232, v232 op_sel_hi:[0,0,0]
	v_mfma_scale_f32_32x32x64_f8f6f4 v[82:97], v[184:191], v[222:229], v[82:97], v232, v232 op_sel_hi:[0,0,0]
	s_setprio 0
	s_barrier
	s_add_i32 s67, s67, s48
	v_lshl_add_u64 v[144:145], s[6:7], 0, v[136:137]
	s_mov_b32 m0, s67
	ds_read_b128 v[198:201], v155 offset:16384
	ds_read_b128 v[206:209], v155 offset:20480
	ds_read_b128 v[202:205], v156 offset:16384
	ds_read_b128 v[210:213], v156 offset:20480
	ds_read_b128 v[214:217], v157 offset:16384
	ds_read_b128 v[222:225], v157 offset:20480
	ds_read_b128 v[218:221], v158 offset:16384
	ds_read_b128 v[226:229], v158 offset:20480
	global_load_lds_dwordx4 v[144:145], off
	s_add_i32 m0, s67, 0x2000
	s_add_u32 s68, s6, 0x4000
	v_lshl_add_u64 v[144:145], s[6:7], 0, v[132:133]
	s_addc_u32 s69, s7, 0
	s_add_i32 s67, s70, s48
	global_load_lds_dwordx4 v[144:145], off
	v_lshl_add_u64 v[144:145], s[68:69], 0, v[136:137]
	s_mov_b32 m0, s67
	v_lshl_add_u64 v[146:147], s[42:43], 0, v[134:135]
	global_load_lds_dwordx4 v[144:145], off
	v_lshl_add_u64 v[144:145], s[68:69], 0, v[132:133]
	s_add_i32 m0, s67, 0x2000
	s_nop 0
	global_load_lds_dwordx4 v[144:145], off
	v_lshl_add_u64 v[144:145], s[42:43], 0, v[138:139]
	s_mov_b32 m0, s31
	s_nop 0
	global_load_lds_dwordx4 v[144:145], off
	s_mov_b32 m0, s39
	s_nop 0
	global_load_lds_dwordx4 v[146:147], off
	s_waitcnt vmcnt(8)
	s_waitcnt lgkmcnt(0)
	s_barrier
	s_setprio 1
	s_waitcnt lgkmcnt(0)
	v_mfma_scale_f32_32x32x64_f8f6f4 v[34:49], v[160:167], v[198:205], 0, v233, v232 op_sel_hi:[0,0,0]
	v_mfma_scale_f32_32x32x64_f8f6f4 v[2:17], v[160:167], v[206:213], 0, v233, v232 op_sel_hi:[0,0,0]
	v_mfma_scale_f32_32x32x64_f8f6f4 v[34:49], v[168:175], v[214:221], v[34:49], v233, v232 op_sel_hi:[0,0,0]
	v_mfma_scale_f32_32x32x64_f8f6f4 v[2:17], v[168:175], v[222:229], v[2:17], v233, v232 op_sel_hi:[0,0,0]
	s_setprio 0
	s_setprio 1
	v_mfma_scale_f32_32x32x64_f8f6f4 v[50:65], v[176:183], v[198:205], 0, v232, v232 op_sel_hi:[0,0,0]
	v_mfma_scale_f32_32x32x64_f8f6f4 v[18:33], v[176:183], v[206:213], 0, v232, v232 op_sel_hi:[0,0,0]
	v_mfma_scale_f32_32x32x64_f8f6f4 v[50:65], v[184:191], v[214:221], v[50:65], v232, v232 op_sel_hi:[0,0,0]
	v_mfma_scale_f32_32x32x64_f8f6f4 v[18:33], v[184:191], v[222:229], v[18:33], v232, v232 op_sel_hi:[0,0,0]
	s_setprio 0
	s_barrier
; #define PG8_STAGE(bufoff, gbase, voff) do { _Pragma("unroll") for (int _i = 0; _i < 2; ++_i) \
;         __builtin_amdgcn_global_load_lds((const unsigned*)((const char*)(gbase) + (voff)[_i]), (PG8_LAS unsigned*)(lds + (bufoff) + ldsw + _i * 8192), 16, 0, 0); } while (0)
; #define PG8_LDA(dst, b, h) do { _Pragma("unroll") for (int m = 0; m < 4; ++m) _Pragma("unroll") for (int k = 0; k < 2; ++k) dst[m][k] = *(const PG8_LAS bf16x8*)(lds + PG8_SA(b, h) + aoff + m * 2048 + k * 1024); } while (0)
; #define PG8_LDB(dst, b, h) do { _Pragma("unroll") for (int n = 0; n < 2; ++n) _Pragma("unroll") for (int k = 0; k < 2; ++k) dst[n][k] = *(const PG8_LAS bf16x8*)(lds + PG8_SB(b, h) + boff + n * 2048 + k * 1024); } while (0)
; #define PG8_MMA(ai, bj, At, Bt) do { __builtin_amdgcn_s_setprio(1); _Pragma("unroll") for (int m = 0; m < 4; ++m) _Pragma("unroll") for (int n = 0; n < 2; ++n) _Pragma("unroll") for (int k = 0; k < 2; ++k) \
;         acc[ai][bj][m][n] = __builtin_amdgcn_mfma_f32_16x16x32_bf16(Bt[n][k], At[m][k], acc[ai][bj][m][n], 0, 0, 0); __builtin_amdgcn_s_setprio(0); } while (0)
; #define PG8_WAIT_V(n) asm volatile("s_waitcnt vmcnt(" #n ")" ::: "memory")
; #define PG8_WAIT_L(n) asm volatile("s_waitcnt lgkmcnt(" #n ")" ::: "memory")
; #define PG8_BAR __builtin_amdgcn_s_barrier()
; #define PG8_SCHED __builtin_amdgcn_sched_barrier(0)
; #define PG8_STAGE(bufoff, gbase, voff) do { _Pragma("unroll") for (int _i = 0; _i < 2; ++_i) \
;         __builtin_amdgcn_global_load_lds((const unsigned*)((const char*)(gbase) + (voff)[_i]), (PG8_LAS unsigned*)(lds + (bufoff) + ldsw + _i * 8192), 16, 0, 0); } while (0)
; template <class Epi, class Sched, int SCW, int SCX, int SCW1 = SCW>
; __device__ __forceinline__ void gemm_phase_f8(PG8_LAS unsigned char* lds, const Gemm g, const Sched& S, const Epi& E, const int tid) {
;     ...
;         for (int t = 0; t < nt; t += 2) {
;     ...
;             PG8_LDB(B0, 1, 0); PG8_LDB(B1, 1, 1); PG8_SCHED; PG8_LDA(At, 1, 0); PG8_STAGE(PG8_SA(0, 1), a2 + hstep, voffA);
;             PG8_WAIT_V(8); PG8_WAIT_L(0); PG8_BAR; PG8_MMA(0, 0, At, B0); PG8_MMA(0, 1, At, B1); PG8_BAR; PG8_SCHED;
;             PG8_LDA(At, 1, 1); PG8_STAGE(PG8_SB(1, 0), b3, voffB); PG8_STAGE(PG8_SB(1, 1), b3 + hstepB, voffB); PG8_STAGE(PG8_SA(1, 0), a3, voffA);
;             PG8_WAIT_V(8); PG8_WAIT_L(0); PG8_BAR; PG8_MMA(1, 0, At, B0); PG8_MMA(1, 1, At, B1); PG8_BAR; PG8_SCHED;
	s_add_i32 s67, 0, 0x18000
	v_add_u32_e32 v148, s67, v131
	v_add_u32_e32 v149, s67, v150
	ds_read_b128 v[160:163], v148
	ds_read_b128 v[164:167], v149
	v_add_u32_e32 v148, s67, v151
	s_add_i32 s68, 0, 0x1c000
	v_add_u32_e32 v149, s67, v152
	ds_read_b128 v[168:171], v148
	ds_read_b128 v[172:175], v149
	v_add_u32_e32 v148, s68, v131
	v_add_u32_e32 v149, s68, v150
	ds_read_b128 v[176:179], v148
	ds_read_b128 v[180:183], v149
	v_add_u32_e32 v148, s68, v151
	v_add_u32_e32 v149, s68, v152
	ds_read_b128 v[184:187], v148
	ds_read_b128 v[188:191], v149
	s_add_u32 s42, s42, 0x40000
	s_addc_u32 s43, s43, 0
	s_mov_b32 m0, s57
	v_lshl_add_u64 v[148:149], s[42:43], 0, v[138:139]
	ds_read_b128 v[198:201], v155 offset:32768
	ds_read_b128 v[206:209], v155 offset:36864
	ds_read_b128 v[202:205], v156 offset:32768
	ds_read_b128 v[210:213], v156 offset:36864
	ds_read_b128 v[214:217], v157 offset:32768
	ds_read_b128 v[222:225], v157 offset:36864
	ds_read_b128 v[218:221], v158 offset:32768
	ds_read_b128 v[226:229], v158 offset:36864
	global_load_lds_dwordx4 v[148:149], off
	v_lshl_add_u64 v[148:149], s[42:43], 0, v[134:135]
	s_mov_b32 m0, s58
	s_nop 0
	global_load_lds_dwordx4 v[148:149], off
	s_waitcnt vmcnt(8)
	s_waitcnt lgkmcnt(0)
	s_barrier
	s_setprio 1
	s_waitcnt lgkmcnt(0)
	v_mfma_scale_f32_32x32x64_f8f6f4 v[98:113], v[160:167], v[198:205], v[98:113], v233, v232 op_sel_hi:[0,0,0]
	v_mfma_scale_f32_32x32x64_f8f6f4 v[66:81], v[160:167], v[206:213], v[66:81], v233, v232 op_sel_hi:[0,0,0]
	v_mfma_scale_f32_32x32x64_f8f6f4 v[98:113], v[168:175], v[214:221], v[98:113], v233, v232 op_sel_hi:[0,0,0]
	v_mfma_scale_f32_32x32x64_f8f6f4 v[66:81], v[168:175], v[222:229], v[66:81], v233, v232 op_sel_hi:[0,0,0]
	s_setprio 0
	s_setprio 1
	v_mfma_scale_f32_32x32x64_f8f6f4 v[114:129], v[176:183], v[198:205], v[114:129], v232, v232 op_sel_hi:[0,0,0]
	v_mfma_scale_f32_32x32x64_f8f6f4 v[82:97], v[176:183], v[206:213], v[82:97], v232, v232 op_sel_hi:[0,0,0]
	v_mfma_scale_f32_32x32x64_f8f6f4 v[114:129], v[184:191], v[214:221], v[114:129], v232, v232 op_sel_hi:[0,0,0]
	v_mfma_scale_f32_32x32x64_f8f6f4 v[82:97], v[184:191], v[222:229], v[82:97], v232, v232 op_sel_hi:[0,0,0]
	s_setprio 0
	s_barrier
	s_add_u32 s42, s6, 0x8000
	s_addc_u32 s43, s7, 0
	s_add_i32 s67, s67, s48
	v_lshl_add_u64 v[148:149], s[42:43], 0, v[136:137]
	s_mov_b32 m0, s67
	ds_read_b128 v[198:201], v155 offset:49152
	ds_read_b128 v[206:209], v155 offset:53248
	ds_read_b128 v[202:205], v156 offset:49152
	ds_read_b128 v[210:213], v156 offset:53248
	ds_read_b128 v[214:217], v157 offset:49152
	ds_read_b128 v[222:225], v157 offset:53248
	ds_read_b128 v[218:221], v158 offset:49152
	ds_read_b128 v[226:229], v158 offset:53248
	global_load_lds_dwordx4 v[148:149], off
	s_add_i32 m0, s67, 0x2000
	s_add_u32 s6, s6, 0xc000
	v_lshl_add_u64 v[148:149], s[42:43], 0, v[132:133]
	s_addc_u32 s7, s7, 0
	s_add_i32 s42, s68, s48
	global_load_lds_dwordx4 v[148:149], off
	v_lshl_add_u64 v[148:149], s[6:7], 0, v[136:137]
	s_mov_b32 m0, s42
	v_lshl_add_u64 v[144:145], v[144:145], 0, s[34:35]
	global_load_lds_dwordx4 v[148:149], off
	v_lshl_add_u64 v[148:149], s[6:7], 0, v[132:133]
	s_add_i32 m0, s42, 0x2000
	s_nop 0
	global_load_lds_dwordx4 v[148:149], off
	s_mov_b32 m0, s59
	s_nop 0
	global_load_lds_dwordx4 v[144:145], off
	v_lshl_add_u64 v[144:145], v[146:147], 0, s[34:35]
	s_mov_b32 m0, s60
	s_nop 0
	global_load_lds_dwordx4 v[144:145], off
	s_waitcnt vmcnt(8)
	s_waitcnt lgkmcnt(0)
	s_barrier
	s_setprio 1
	s_waitcnt lgkmcnt(0)
	v_mfma_scale_f32_32x32x64_f8f6f4 v[34:49], v[160:167], v[198:205], v[34:49], v233, v232 op_sel_hi:[0,0,0]
	v_mfma_scale_f32_32x32x64_f8f6f4 v[2:17], v[160:167], v[206:213], v[2:17], v233, v232 op_sel_hi:[0,0,0]
	v_mfma_scale_f32_32x32x64_f8f6f4 v[34:49], v[168:175], v[214:221], v[34:49], v233, v232 op_sel_hi:[0,0,0]
	v_mfma_scale_f32_32x32x64_f8f6f4 v[2:17], v[168:175], v[222:229], v[2:17], v233, v232 op_sel_hi:[0,0,0]
	s_setprio 0
	s_setprio 1
	v_mfma_scale_f32_32x32x64_f8f6f4 v[50:65], v[176:183], v[198:205], v[50:65], v232, v232 op_sel_hi:[0,0,0]
	v_mfma_scale_f32_32x32x64_f8f6f4 v[18:33], v[176:183], v[206:213], v[18:33], v232, v232 op_sel_hi:[0,0,0]
	v_mfma_scale_f32_32x32x64_f8f6f4 v[50:65], v[184:191], v[214:221], v[50:65], v232, v232 op_sel_hi:[0,0,0]
	v_mfma_scale_f32_32x32x64_f8f6f4 v[18:33], v[184:191], v[222:229], v[18:33], v232, v232 op_sel_hi:[0,0,0]
	s_setprio 0
	s_barrier
	s_add_i32 s66, s66, 2
	s_add_u32 s64, s64, 0x10000
	s_addc_u32 s65, s65, 0
	s_add_u32 s40, s40, 0x100
	s_addc_u32 s41, s41, 0
	s_cmp_gt_u32 s66, 13
	s_cbranch_scc1 .Lpeel_exit_1896

; #define PG8_BAR __builtin_amdgcn_s_barrier()
; #define PG8_BAR __builtin_amdgcn_s_barrier()
; template <class Epi, class Sched, int SCW, int SCX, int SCW1 = SCW>
; __device__ __forceinline__ void gemm_phase_f8(PG8_LAS unsigned char* lds, const Gemm g, const Sched& S, const Epi& E, const int tid) {
;     ...
;         if (wr == 0) PG8_BAR;
.Lpeel_exit_1896:
	s_and_b64 vcc, exec, s[8:9]
	s_cbranch_vccz .LBB0_1899
	s_barrier

; #define PG8_STAGE(bufoff, gbase, voff) do { _Pragma("unroll") for (int _i = 0; _i < 2; ++_i) \
;         __builtin_amdgcn_global_load_lds((const unsigned*)((const char*)(gbase) + (voff)[_i]), (PG8_LAS unsigned*)(lds + (bufoff) + ldsw + _i * 8192), 16, 0, 0); } while (0)
; #define PG8_LDA(dst, b, h) do { _Pragma("unroll") for (int m = 0; m < 4; ++m) _Pragma("unroll") for (int k = 0; k < 2; ++k) dst[m][k] = *(const PG8_LAS bf16x8*)(lds + PG8_SA(b, h) + aoff + m * 2048 + k * 1024); } while (0)
; #define PG8_LDB(dst, b, h) do { _Pragma("unroll") for (int n = 0; n < 2; ++n) _Pragma("unroll") for (int k = 0; k < 2; ++k) dst[n][k] = *(const PG8_LAS bf16x8*)(lds + PG8_SB(b, h) + boff + n * 2048 + k * 1024); } while (0)
; #define PG8_MMA(ai, bj, At, Bt) do { __builtin_amdgcn_s_setprio(1); _Pragma("unroll") for (int m = 0; m < 4; ++m) _Pragma("unroll") for (int n = 0; n < 2; ++n) _Pragma("unroll") for (int k = 0; k < 2; ++k) \
;         acc[ai][bj][m][n] = __builtin_amdgcn_mfma_f32_16x16x32_bf16(Bt[n][k], At[m][k], acc[ai][bj][m][n], 0, 0, 0); __builtin_amdgcn_s_setprio(0); } while (0)
; #define PG8_WAIT_V(n) asm volatile("s_waitcnt vmcnt(" #n ")" ::: "memory")
; #define PG8_WAIT_L(n) asm volatile("s_waitcnt lgkmcnt(" #n ")" ::: "memory")
; template <class Epi, class Sched, int SCW, int SCX, int SCW1 = SCW>
; __device__ __forceinline__ void gemm_phase_f8(PG8_LAS unsigned char* lds, const Gemm g, const Sched& S, const Epi& E, const int tid) {
;     ...
;         for (int t = 0; t < nt; t += 2) {
;             const bool last = (t == nt - 2);
;             const char* a1 = cA + (size_t)(t + 1) * kstep;
;             const char* a2 = last ? nA : cA + (size_t)(t + 2) * kstep; const char* b2 = last ? nB : cB + (size_t)(t + 2) * kstepB;
;             const char* a3 = a2 + kstep; const char* b3 = b2 + kstepB;
;             if (last && has_next) S.a_ready(nxt);
;             PG8_LDB(B0, 0, 0); PG8_LDB(B1, 0, 1); PG8_SCHED; PG8_LDA(At, 0, 0); PG8_STAGE(PG8_SA(1, 1), a1 + hstep, voffA);
;             PG8_WAIT_V(8); PG8_WAIT_L(0); PG8_BAR; PG8_MMA(0, 0, At, B0); PG8_MMA(0, 1, At, B1); PG8_BAR; PG8_SCHED;
;             PG8_LDA(At, 0, 1); PG8_STAGE(PG8_SB(0, 0), b2, voffB); PG8_STAGE(PG8_SB(0, 1), b2 + hstepB, voffB); PG8_STAGE(PG8_SA(0, 0), a2, voffA);
;             PG8_WAIT_V(8); PG8_WAIT_L(0); PG8_BAR; PG8_MMA(1, 0, At, B0); PG8_MMA(1, 1, At, B1); PG8_BAR; PG8_SCHED;
.LBB0_1999:
	s_add_i32 s12, s24, -2
	s_add_u32 s13, s6, 0x10000
	s_addc_u32 s17, s7, 0
	s_add_u32 s28, s28, 0xc000
	v_mov_b32_e32 v2, 0
	s_addc_u32 s29, s29, 0
	s_mov_b32 s6, 0
	s_add_i32 s63, s6, 2
	s_add_u32 s7, s28, 0x4000
	s_addc_u32 s30, s29, 0
	s_add_i32 s66, 0, 0x10000
	s_cmp_eq_u32 s12, s6
	v_add_u32_e32 v153, s66, v131
	v_add_u32_e32 v158, s66, v144
	s_cselect_b32 s31, s21, s30
	s_cselect_b32 s30, s20, s7
	ds_read_b128 v[154:157], v153
	ds_read_b128 v[158:161], v158
	v_add_u32_e32 v153, s66, v145
	v_add_u32_e32 v166, s66, v146
	s_cselect_b32 s7, s23, s17
	s_cselect_b32 s6, s22, s13
	s_add_i32 s87, 0, 0x14000
	ds_read_b128 v[162:165], v153
	ds_read_b128 v[166:169], v166
	v_add_u32_e32 v153, s87, v131
	v_add_u32_e32 v174, s87, v144
	ds_read_b128 v[170:173], v153
	ds_read_b128 v[174:177], v174
	v_add_u32_e32 v153, s87, v145
	v_add_u32_e32 v182, s87, v146
	ds_read_b128 v[178:181], v153
	ds_read_b128 v[182:185], v182
	v_lshl_add_u64 v[194:195], s[28:29], 0, v[140:141]
	s_add_i32 m0, s51, 0xc000
	ds_read_b128 v[186:189], v149
	ds_read_b128 v[198:201], v149 offset:4096
	ds_read_b128 v[190:193], v150
	ds_read_b128 v[202:205], v150 offset:4096
	ds_read_b128 v[206:209], v151
	ds_read_b128 v[214:217], v151 offset:4096
	ds_read_b128 v[210:213], v152
	ds_read_b128 v[218:221], v152 offset:4096
	global_load_lds_dwordx4 v[194:195], off
	v_lshl_add_u64 v[194:195], s[28:29], 0, v[142:143]
	s_add_i32 m0, s51, 0xe000
	s_nop 0
	global_load_lds_dwordx4 v[194:195], off
	s_waitcnt vmcnt(8)
	s_waitcnt lgkmcnt(0)
	s_barrier
	s_setprio 1
	s_waitcnt lgkmcnt(0)
	v_mfma_scale_f32_32x32x64_f8f6f4 v[114:129], v[154:161], v[186:193], 0, v233, v234 op_sel_hi:[0,0,0]
	v_mfma_scale_f32_32x32x64_f8f6f4 v[82:97], v[154:161], v[198:205], 0, v233, v234 op_sel_hi:[0,0,0]
	v_mfma_scale_f32_32x32x64_f8f6f4 v[114:129], v[162:169], v[206:213], v[114:129], v233, v234 op_sel_hi:[0,0,0]
	v_mfma_scale_f32_32x32x64_f8f6f4 v[82:97], v[162:169], v[214:221], v[82:97], v233, v234 op_sel_hi:[0,0,0]
	s_setprio 0
	s_setprio 1
	v_mfma_scale_f32_32x32x64_f8f6f4 v[98:113], v[170:177], v[186:193], 0, v233, v234 op_sel_hi:[0,0,0]
	v_mfma_scale_f32_32x32x64_f8f6f4 v[66:81], v[170:177], v[198:205], 0, v233, v234 op_sel_hi:[0,0,0]
	v_mfma_scale_f32_32x32x64_f8f6f4 v[98:113], v[178:185], v[206:213], v[98:113], v233, v234 op_sel_hi:[0,0,0]
	v_mfma_scale_f32_32x32x64_f8f6f4 v[66:81], v[178:185], v[214:221], v[66:81], v233, v234 op_sel_hi:[0,0,0]
	s_setprio 0
	s_barrier
	s_add_i32 s66, s66, s50
	v_lshl_add_u64 v[194:195], s[6:7], 0, v[134:135]
	s_mov_b32 m0, s66
	ds_read_b128 v[186:189], v149 offset:16384
	ds_read_b128 v[198:201], v149 offset:20480
	ds_read_b128 v[190:193], v150 offset:16384
	ds_read_b128 v[202:205], v150 offset:20480
	ds_read_b128 v[206:209], v151 offset:16384
	ds_read_b128 v[214:217], v151 offset:20480
	ds_read_b128 v[210:213], v152 offset:16384
	ds_read_b128 v[218:221], v152 offset:20480
	global_load_lds_dwordx4 v[194:195], off
	s_add_i32 m0, s66, 0x2000
	s_add_u32 s88, s6, 0x4000
	v_lshl_add_u64 v[194:195], s[6:7], 0, v[138:139]
	s_addc_u32 s89, s7, 0
	s_add_i32 s66, s87, s50
	global_load_lds_dwordx4 v[194:195], off
	v_lshl_add_u64 v[194:195], s[88:89], 0, v[134:135]
	s_mov_b32 m0, s66
	v_lshl_add_u64 v[222:223], s[30:31], 0, v[136:137]
	global_load_lds_dwordx4 v[194:195], off
	v_lshl_add_u64 v[194:195], s[88:89], 0, v[138:139]
	s_add_i32 m0, s66, 0x2000
	s_nop 0
	global_load_lds_dwordx4 v[194:195], off
	v_lshl_add_u64 v[194:195], s[30:31], 0, v[132:133]
	s_mov_b32 m0, s51
	s_nop 0
	global_load_lds_dwordx4 v[194:195], off
	s_mov_b32 m0, s52
	s_nop 0
	global_load_lds_dwordx4 v[222:223], off
	s_waitcnt vmcnt(8)
	s_waitcnt lgkmcnt(0)
	s_barrier
	s_setprio 1
	s_waitcnt lgkmcnt(0)
	v_mfma_scale_f32_32x32x64_f8f6f4 v[50:65], v[154:161], v[186:193], 0, v233, v234 op_sel_hi:[0,0,0]
	v_mfma_scale_f32_32x32x64_f8f6f4 v[18:33], v[154:161], v[198:205], 0, v233, v234 op_sel_hi:[0,0,0]
	v_mfma_scale_f32_32x32x64_f8f6f4 v[50:65], v[162:169], v[206:213], v[50:65], v233, v234 op_sel_hi:[0,0,0]
	v_mfma_scale_f32_32x32x64_f8f6f4 v[18:33], v[162:169], v[214:221], v[18:33], v233, v234 op_sel_hi:[0,0,0]
	s_setprio 0
	s_setprio 1
	v_mfma_scale_f32_32x32x64_f8f6f4 v[34:49], v[170:177], v[186:193], 0, v233, v234 op_sel_hi:[0,0,0]
	v_mfma_scale_f32_32x32x64_f8f6f4 v[2:17], v[170:177], v[198:205], 0, v233, v234 op_sel_hi:[0,0,0]
	v_mfma_scale_f32_32x32x64_f8f6f4 v[34:49], v[178:185], v[206:213], v[34:49], v233, v234 op_sel_hi:[0,0,0]
	v_mfma_scale_f32_32x32x64_f8f6f4 v[2:17], v[178:185], v[214:221], v[2:17], v233, v234 op_sel_hi:[0,0,0]
	s_setprio 0
	s_barrier
; #define PG8_STAGE(bufoff, gbase, voff) do { _Pragma("unroll") for (int _i = 0; _i < 2; ++_i) \
;         __builtin_amdgcn_global_load_lds((const unsigned*)((const char*)(gbase) + (voff)[_i]), (PG8_LAS unsigned*)(lds + (bufoff) + ldsw + _i * 8192), 16, 0, 0); } while (0)
; #define PG8_LDA(dst, b, h) do { _Pragma("unroll") for (int m = 0; m < 4; ++m) _Pragma("unroll") for (int k = 0; k < 2; ++k) dst[m][k] = *(const PG8_LAS bf16x8*)(lds + PG8_SA(b, h) + aoff + m * 2048 + k * 1024); } while (0)
; #define PG8_LDB(dst, b, h) do { _Pragma("unroll") for (int n = 0; n < 2; ++n) _Pragma("unroll") for (int k = 0; k < 2; ++k) dst[n][k] = *(const PG8_LAS bf16x8*)(lds + PG8_SB(b, h) + boff + n * 2048 + k * 1024); } while (0)
; #define PG8_MMA(ai, bj, At, Bt) do { __builtin_amdgcn_s_setprio(1); _Pragma("unroll") for (int m = 0; m < 4; ++m) _Pragma("unroll") for (int n = 0; n < 2; ++n) _Pragma("unroll") for (int k = 0; k < 2; ++k) \
;         acc[ai][bj][m][n] = __builtin_amdgcn_mfma_f32_16x16x32_bf16(Bt[n][k], At[m][k], acc[ai][bj][m][n], 0, 0, 0); __builtin_amdgcn_s_setprio(0); } while (0)
; #define PG8_WAIT_V(n) asm volatile("s_waitcnt vmcnt(" #n ")" ::: "memory")
; #define PG8_WAIT_L(n) asm volatile("s_waitcnt lgkmcnt(" #n ")" ::: "memory")
; #define PG8_BAR __builtin_amdgcn_s_barrier()
; #define PG8_SCHED __builtin_amdgcn_sched_barrier(0)
; #define PG8_STAGE(bufoff, gbase, voff) do { _Pragma("unroll") for (int _i = 0; _i < 2; ++_i) \
;         __builtin_amdgcn_global_load_lds((const unsigned*)((const char*)(gbase) + (voff)[_i]), (PG8_LAS unsigned*)(lds + (bufoff) + ldsw + _i * 8192), 16, 0, 0); } while (0)
; template <class Epi, class Sched, int SCW, int SCX, int SCW1 = SCW>
; __device__ __forceinline__ void gemm_phase_f8(PG8_LAS unsigned char* lds, const Gemm g, const Sched& S, const Epi& E, const int tid) {
;     ...
;         for (int t = 0; t < nt; t += 2) {
;     ...
;             PG8_LDB(B0, 1, 0); PG8_LDB(B1, 1, 1); PG8_SCHED; PG8_LDA(At, 1, 0); PG8_STAGE(PG8_SA(0, 1), a2 + hstep, voffA);
;             PG8_WAIT_V(8); PG8_WAIT_L(0); PG8_BAR; PG8_MMA(0, 0, At, B0); PG8_MMA(0, 1, At, B1); PG8_BAR; PG8_SCHED;
;             PG8_LDA(At, 1, 1); PG8_STAGE(PG8_SB(1, 0), b3, voffB); PG8_STAGE(PG8_SB(1, 1), b3 + hstepB, voffB); PG8_STAGE(PG8_SA(1, 0), a3, voffA);
;             PG8_WAIT_V(8); PG8_WAIT_L(0); PG8_BAR; PG8_MMA(1, 0, At, B0); PG8_MMA(1, 1, At, B1); PG8_BAR; PG8_SCHED;
	s_add_i32 s66, 0, 0x18000
	v_add_u32_e32 v153, s66, v131
	v_add_u32_e32 v158, s66, v144
	ds_read_b128 v[154:157], v153
	ds_read_b128 v[158:161], v158
	v_add_u32_e32 v153, s66, v145
	v_add_u32_e32 v166, s66, v146
	s_add_i32 s87, 0, 0x1c000
	ds_read_b128 v[162:165], v153
	ds_read_b128 v[166:169], v166
	v_add_u32_e32 v153, s87, v131
	v_add_u32_e32 v174, s87, v144
	ds_read_b128 v[170:173], v153
	ds_read_b128 v[174:177], v174
	v_add_u32_e32 v153, s87, v145
	v_add_u32_e32 v182, s87, v146
	ds_read_b128 v[178:181], v153
	ds_read_b128 v[182:185], v182
	s_add_u32 s30, s30, 0x4000
	s_addc_u32 s31, s31, 0
	s_mov_b32 m0, s53
	v_lshl_add_u64 v[224:225], s[30:31], 0, v[132:133]
	ds_read_b128 v[186:189], v149 offset:32768
	ds_read_b128 v[198:201], v149 offset:36864
	ds_read_b128 v[190:193], v150 offset:32768
	ds_read_b128 v[202:205], v150 offset:36864
	ds_read_b128 v[206:209], v151 offset:32768
	ds_read_b128 v[214:217], v151 offset:36864
	ds_read_b128 v[210:213], v152 offset:32768
	ds_read_b128 v[218:221], v152 offset:36864
	global_load_lds_dwordx4 v[224:225], off
	v_lshl_add_u64 v[224:225], s[30:31], 0, v[136:137]
	s_mov_b32 m0, s54
	s_nop 0
	global_load_lds_dwordx4 v[224:225], off
	s_waitcnt vmcnt(8)
	s_waitcnt lgkmcnt(0)
	s_barrier
	s_setprio 1
	s_waitcnt lgkmcnt(0)
	v_mfma_scale_f32_32x32x64_f8f6f4 v[114:129], v[154:161], v[186:193], v[114:129], v233, v234 op_sel_hi:[0,0,0]
	v_mfma_scale_f32_32x32x64_f8f6f4 v[82:97], v[154:161], v[198:205], v[82:97], v233, v234 op_sel_hi:[0,0,0]
	v_mfma_scale_f32_32x32x64_f8f6f4 v[114:129], v[162:169], v[206:213], v[114:129], v233, v234 op_sel_hi:[0,0,0]
	v_mfma_scale_f32_32x32x64_f8f6f4 v[82:97], v[162:169], v[214:221], v[82:97], v233, v234 op_sel_hi:[0,0,0]
	s_setprio 0
	s_setprio 1
	v_mfma_scale_f32_32x32x64_f8f6f4 v[98:113], v[170:177], v[186:193], v[98:113], v233, v234 op_sel_hi:[0,0,0]
	v_mfma_scale_f32_32x32x64_f8f6f4 v[66:81], v[170:177], v[198:205], v[66:81], v233, v234 op_sel_hi:[0,0,0]
	v_mfma_scale_f32_32x32x64_f8f6f4 v[98:113], v[178:185], v[206:213], v[98:113], v233, v234 op_sel_hi:[0,0,0]
	v_mfma_scale_f32_32x32x64_f8f6f4 v[66:81], v[178:185], v[214:221], v[66:81], v233, v234 op_sel_hi:[0,0,0]
	s_setprio 0
	s_barrier
	s_add_u32 s30, s6, 0x8000
	s_addc_u32 s31, s7, 0
	s_add_i32 s66, s66, s50
	v_lshl_add_u64 v[224:225], s[30:31], 0, v[134:135]
	s_mov_b32 m0, s66
	ds_read_b128 v[186:189], v149 offset:49152
	ds_read_b128 v[198:201], v149 offset:53248
	ds_read_b128 v[190:193], v150 offset:49152
	ds_read_b128 v[202:205], v150 offset:53248
	ds_read_b128 v[206:209], v151 offset:49152
	ds_read_b128 v[214:217], v151 offset:53248
	ds_read_b128 v[210:213], v152 offset:49152
	ds_read_b128 v[218:221], v152 offset:53248
	global_load_lds_dwordx4 v[224:225], off
	s_add_i32 m0, s66, 0x2000
	s_add_u32 s6, s6, 0xc000
	v_lshl_add_u64 v[224:225], s[30:31], 0, v[138:139]
	s_addc_u32 s7, s7, 0
	s_add_i32 s30, s87, s50
	global_load_lds_dwordx4 v[224:225], off
	v_lshl_add_u64 v[224:225], s[6:7], 0, v[134:135]
	s_mov_b32 m0, s30
	v_lshl_add_u64 v[194:195], v[194:195], 0, s[100:101]
	global_load_lds_dwordx4 v[224:225], off
	v_lshl_add_u64 v[224:225], s[6:7], 0, v[138:139]
	s_add_i32 m0, s30, 0x2000
	s_nop 0
	global_load_lds_dwordx4 v[224:225], off
	s_mov_b32 m0, s59
	s_nop 0
	global_load_lds_dwordx4 v[194:195], off
	v_lshl_add_u64 v[194:195], v[222:223], 0, s[100:101]
	s_mov_b32 m0, s60
	s_nop 0
	global_load_lds_dwordx4 v[194:195], off
	s_waitcnt vmcnt(8)
	s_waitcnt lgkmcnt(0)
	s_barrier
	s_setprio 1
	s_waitcnt lgkmcnt(0)
	v_mfma_scale_f32_32x32x64_f8f6f4 v[50:65], v[154:161], v[186:193], v[50:65], v233, v234 op_sel_hi:[0,0,0]
	v_mfma_scale_f32_32x32x64_f8f6f4 v[18:33], v[154:161], v[198:205], v[18:33], v233, v234 op_sel_hi:[0,0,0]
	v_mfma_scale_f32_32x32x64_f8f6f4 v[50:65], v[162:169], v[206:213], v[50:65], v233, v234 op_sel_hi:[0,0,0]
	v_mfma_scale_f32_32x32x64_f8f6f4 v[18:33], v[162:169], v[214:221], v[18:33], v233, v234 op_sel_hi:[0,0,0]
	s_setprio 0
	s_setprio 1
	v_mfma_scale_f32_32x32x64_f8f6f4 v[34:49], v[170:177], v[186:193], v[34:49], v233, v234 op_sel_hi:[0,0,0]
	v_mfma_scale_f32_32x32x64_f8f6f4 v[2:17], v[170:177], v[198:205], v[2:17], v233, v234 op_sel_hi:[0,0,0]
	v_mfma_scale_f32_32x32x64_f8f6f4 v[34:49], v[178:185], v[206:213], v[34:49], v233, v234 op_sel_hi:[0,0,0]
	v_mfma_scale_f32_32x32x64_f8f6f4 v[2:17], v[178:185], v[214:221], v[2:17], v233, v234 op_sel_hi:[0,0,0]
	s_setprio 0
	s_barrier
	s_add_u32 s13, s13, 0x10000
	s_addc_u32 s17, s17, 0
	s_add_u32 s28, s28, 0x10000
	s_addc_u32 s29, s29, 0
	s_cmp_ge_i32 s63, s24
	s_mov_b32 s6, s63
	s_cbranch_scc1 .Lpeel_exit_2000

; #define PG8_STAGE(bufoff, gbase, voff) do { _Pragma("unroll") for (int _i = 0; _i < 2; ++_i) \
;         __builtin_amdgcn_global_load_lds((const unsigned*)((const char*)(gbase) + (voff)[_i]), (PG8_LAS unsigned*)(lds + (bufoff) + ldsw + _i * 8192), 16, 0, 0); } while (0)
; #define PG8_LDA(dst, b, h) do { _Pragma("unroll") for (int m = 0; m < 4; ++m) _Pragma("unroll") for (int k = 0; k < 2; ++k) dst[m][k] = *(const PG8_LAS bf16x8*)(lds + PG8_SA(b, h) + aoff + m * 2048 + k * 1024); } while (0)
; #define PG8_LDB(dst, b, h) do { _Pragma("unroll") for (int n = 0; n < 2; ++n) _Pragma("unroll") for (int k = 0; k < 2; ++k) dst[n][k] = *(const PG8_LAS bf16x8*)(lds + PG8_SB(b, h) + boff + n * 2048 + k * 1024); } while (0)
; #define PG8_WAIT_V(n) asm volatile("s_waitcnt vmcnt(" #n ")" ::: "memory")
; #define PG8_WAIT_L(n) asm volatile("s_waitcnt lgkmcnt(" #n ")" ::: "memory")
; #define PG8_BAR __builtin_amdgcn_s_barrier()
; #define PG8_SCHED __builtin_amdgcn_sched_barrier(0)
; #define PG8_WAIT_V(n) asm volatile("s_waitcnt vmcnt(" #n ")" ::: "memory")
; template <class Epi, class Sched, bool ALIGN_EPI = false, bool SP2 = false>
; __device__ __forceinline__ void gemm_phase(PG8_LAS unsigned char* lds, const Gemm g, const Sched& S, const Epi& E, const int tid) {
;     ...
;         const bool has_next = S.next(ui + 1, nxt);
;         const char* nA = has_next ? (const char*)g.A + (size_t)nxt.pm * tstep + (size_t)nxt.k0 * 2 : cA; const char* nB = has_next ? (const char*)g.Bt + (size_t)nxt.pn * tstep + (size_t)nxt.k0 * 2 : cB;
;         for (int t = 0; t < nt; t += 2) {
;             const bool last = (t == nt - 2);
;             const char* a1 = cA + (size_t)(t + 1) * kstep;
;             const char* a2 = last ? nA : cA + (size_t)(t + 2) * kstep; const char* b2 = last ? nB : cB + (size_t)(t + 2) * kstep;
;             const char* a3 = a2 + kstep; const char* b3 = b2 + kstep;
;             if (last && has_next) S.a_ready(nxt);
;             if constexpr (SP2) {
;             PG8_LDB(B0, 0, 0); PG8_LDB(B1, 0, 1); PG8_SCHED; PG8_LDA(At, 0, 0); PG8_STAGE(PG8_SA(1, 1), a1 + hstep, voffA);
;             PG8_WAIT_V(8); PG8_WAIT_L(0); PG8_BAR; PG8_MMA(0, 0, At, B0); PG8_MMA(0, 1, At, B1); PG8_BAR; PG8_SCHED;
;             PG8_LDA(At, 0, 1); PG8_STAGE(PG8_SB(0, 0), b2, voffB); PG8_STAGE(PG8_SB(0, 1), b2 + hstep, voffB); PG8_STAGE(PG8_SA(0, 0), a2, voffA);
.LBB0_2281:
	s_ashr_i32 s47, s46, 31
	s_lshl_b64 s[12:13], s[46:47], 20
	s_add_u32 s50, s58, s12
	s_addc_u32 s51, s59, s13
	s_and_b64 s[12:13], s[48:49], exec
	s_cselect_b32 s5, s51, s55
	s_cselect_b32 s12, s50, s54
	s_ashr_i32 s31, s30, 31
	s_lshl_b64 s[18:19], s[30:31], 20
	s_add_u32 s52, s60, s18
	s_addc_u32 s53, s61, s19
	s_and_b64 s[18:19], s[48:49], exec
	s_cselect_b32 s13, s53, s7
	s_cselect_b32 s15, s52, s6
	s_add_u32 s54, s54, 0x80080
	s_addc_u32 s55, s55, 0
	s_add_u32 s18, s6, 0x100
	s_waitcnt vmcnt(0)
	v_mov_b32_e32 v6, 0
	s_addc_u32 s19, s7, 0
	s_mov_b32 s24, -2
	s_add_u32 s6, s54, 0xfff80080
	s_addc_u32 s7, s55, -1
	s_add_i32 s26, 0, 0x10000
	s_cmp_eq_u32 s24, 28
	s_cselect_b32 s57, s5, s7
	s_cselect_b32 s56, s12, s6
	v_add_u32_e32 v131, s26, v156
	s_cselect_b32 s7, s13, s19
	s_cselect_b32 s6, s15, s18
	s_add_i32 s31, 0, 0x14000
	ds_read_b128 v[172:175], v131
	ds_read_b128 v[176:179], v131 offset:1024
	ds_read_b128 v[180:183], v131 offset:2048
	ds_read_b128 v[184:187], v131 offset:3072
	v_add_u32_e32 v131, s31, v156
	ds_read_b128 v[188:191], v131
	ds_read_b128 v[192:195], v131 offset:1024
	ds_read_b128 v[198:201], v131 offset:2048
	ds_read_b128 v[202:205], v131 offset:3072
	v_lshl_add_u64 v[132:133], s[54:55], 0, v[148:149]
	s_add_i32 m0, s65, 0xc000
	ds_read_b128 v[206:209], v170
	ds_read_b128 v[210:213], v170 offset:1024
	ds_read_b128 v[214:217], v170 offset:2048
	ds_read_b128 v[218:221], v170 offset:3072
	ds_read_b128 v[222:225], v170 offset:4096
	ds_read_b128 v[226:229], v170 offset:5120
	ds_read_b128 v[244:247], v170 offset:6144
	ds_read_b128 v[248:251], v170 offset:7168
	global_load_lds_dwordx4 v[132:133], off
	v_lshl_add_u64 v[132:133], s[54:55], 0, v[150:151]
	s_add_i32 m0, s65, 0xe000
	s_nop 0
	global_load_lds_dwordx4 v[132:133], off
	s_waitcnt vmcnt(8)
	s_waitcnt lgkmcnt(0)
	s_barrier
	s_setprio 1
	s_waitcnt lgkmcnt(0)
	v_mfma_f32_16x16x32_bf16 v[122:125], v[172:175], v[206:209], 0
	v_mfma_f32_16x16x32_bf16 v[114:117], v[180:183], v[206:209], 0
	v_mfma_f32_16x16x32_bf16 v[106:109], v[172:175], v[214:217], 0
	v_mfma_f32_16x16x32_bf16 v[98:101], v[180:183], v[214:217], 0
	v_mfma_f32_16x16x32_bf16 v[90:93], v[172:175], v[222:225], 0
	v_mfma_f32_16x16x32_bf16 v[82:85], v[180:183], v[222:225], 0
	v_mfma_f32_16x16x32_bf16 v[74:77], v[172:175], v[244:247], 0
	v_mfma_f32_16x16x32_bf16 v[66:69], v[180:183], v[244:247], 0
	v_mfma_f32_16x16x32_bf16 v[122:125], v[176:179], v[210:213], v[122:125]
	v_mfma_f32_16x16x32_bf16 v[114:117], v[184:187], v[210:213], v[114:117]
	v_mfma_f32_16x16x32_bf16 v[106:109], v[176:179], v[218:221], v[106:109]
	v_mfma_f32_16x16x32_bf16 v[98:101], v[184:187], v[218:221], v[98:101]
	v_mfma_f32_16x16x32_bf16 v[90:93], v[176:179], v[226:229], v[90:93]
	v_mfma_f32_16x16x32_bf16 v[82:85], v[184:187], v[226:229], v[82:85]
	v_mfma_f32_16x16x32_bf16 v[74:77], v[176:179], v[248:251], v[74:77]
	v_mfma_f32_16x16x32_bf16 v[66:69], v[184:187], v[248:251], v[66:69]
	s_setprio 0
	s_setprio 1
	v_mfma_f32_16x16x32_bf16 v[126:129], v[188:191], v[206:209], 0
	v_mfma_f32_16x16x32_bf16 v[118:121], v[198:201], v[206:209], 0
	v_mfma_f32_16x16x32_bf16 v[110:113], v[188:191], v[214:217], 0
	v_mfma_f32_16x16x32_bf16 v[102:105], v[198:201], v[214:217], 0
	v_mfma_f32_16x16x32_bf16 v[94:97], v[188:191], v[222:225], 0
	v_mfma_f32_16x16x32_bf16 v[86:89], v[198:201], v[222:225], 0
	v_mfma_f32_16x16x32_bf16 v[78:81], v[188:191], v[244:247], 0
	v_mfma_f32_16x16x32_bf16 v[70:73], v[198:201], v[244:247], 0
	v_mfma_f32_16x16x32_bf16 v[126:129], v[192:195], v[210:213], v[126:129]
	v_mfma_f32_16x16x32_bf16 v[118:121], v[202:205], v[210:213], v[118:121]
	v_mfma_f32_16x16x32_bf16 v[110:113], v[192:195], v[218:221], v[110:113]
	v_mfma_f32_16x16x32_bf16 v[102:105], v[202:205], v[218:221], v[102:105]
	v_mfma_f32_16x16x32_bf16 v[94:97], v[192:195], v[226:229], v[94:97]
	v_mfma_f32_16x16x32_bf16 v[86:89], v[202:205], v[226:229], v[86:89]
	v_mfma_f32_16x16x32_bf16 v[78:81], v[192:195], v[248:251], v[78:81]
	v_mfma_f32_16x16x32_bf16 v[70:73], v[202:205], v[248:251], v[70:73]
	s_setprio 0
	s_barrier
	s_add_i32 s26, s26, s64
	v_lshl_add_u64 v[132:133], s[6:7], 0, v[136:137]
	s_mov_b32 m0, s26
	ds_read_b128 v[206:209], v170 offset:16384
	ds_read_b128 v[210:213], v170 offset:17408
	ds_read_b128 v[214:217], v170 offset:18432
	ds_read_b128 v[218:221], v170 offset:19456
	ds_read_b128 v[222:225], v170 offset:20480
	ds_read_b128 v[226:229], v170 offset:21504
	ds_read_b128 v[244:247], v170 offset:22528
	ds_read_b128 v[248:251], v170 offset:23552
	global_load_lds_dwordx4 v[132:133], off
	s_add_i32 m0, s26, 0x2000
	s_add_u32 s36, s6, 0x80000
	v_lshl_add_u64 v[152:153], s[6:7], 0, v[140:141]
	s_addc_u32 s37, s7, 0
	s_add_i32 s26, s31, s64
	global_load_lds_dwordx4 v[152:153], off
	v_lshl_add_u64 v[230:231], s[36:37], 0, v[136:137]
	s_mov_b32 m0, s26
	v_lshl_add_u64 v[242:243], s[56:57], 0, v[138:139]
	global_load_lds_dwordx4 v[230:231], off
	v_lshl_add_u64 v[230:231], s[36:37], 0, v[140:141]
	s_add_i32 m0, s26, 0x2000
	s_nop 0
	global_load_lds_dwordx4 v[230:231], off
	v_lshl_add_u64 v[230:231], s[56:57], 0, v[134:135]
	s_mov_b32 m0, s65
	s_nop 0
	global_load_lds_dwordx4 v[230:231], off
	s_mov_b32 m0, s68
	s_nop 0
	global_load_lds_dwordx4 v[242:243], off
	s_waitcnt vmcnt(8)
	s_waitcnt lgkmcnt(0)
	s_barrier
; #define PG8_STAGE(bufoff, gbase, voff) do { _Pragma("unroll") for (int _i = 0; _i < 2; ++_i) \
;         __builtin_amdgcn_global_load_lds((const unsigned*)((const char*)(gbase) + (voff)[_i]), (PG8_LAS unsigned*)(lds + (bufoff) + ldsw + _i * 8192), 16, 0, 0); } while (0)
; #define PG8_LDA(dst, b, h) do { _Pragma("unroll") for (int m = 0; m < 4; ++m) _Pragma("unroll") for (int k = 0; k < 2; ++k) dst[m][k] = *(const PG8_LAS bf16x8*)(lds + PG8_SA(b, h) + aoff + m * 2048 + k * 1024); } while (0)
; #define PG8_LDB(dst, b, h) do { _Pragma("unroll") for (int n = 0; n < 2; ++n) _Pragma("unroll") for (int k = 0; k < 2; ++k) dst[n][k] = *(const PG8_LAS bf16x8*)(lds + PG8_SB(b, h) + boff + n * 2048 + k * 1024); } while (0)
; #define PG8_MMA(ai, bj, At, Bt) do { __builtin_amdgcn_s_setprio(1); _Pragma("unroll") for (int m = 0; m < 4; ++m) _Pragma("unroll") for (int n = 0; n < 2; ++n) _Pragma("unroll") for (int k = 0; k < 2; ++k) \
;         acc[ai][bj][m][n] = __builtin_amdgcn_mfma_f32_16x16x32_bf16(Bt[n][k], At[m][k], acc[ai][bj][m][n], 0, 0, 0); __builtin_amdgcn_s_setprio(0); } while (0)
; #define PG8_WAIT_V(n) asm volatile("s_waitcnt vmcnt(" #n ")" ::: "memory")
; #define PG8_WAIT_L(n) asm volatile("s_waitcnt lgkmcnt(" #n ")" ::: "memory")
; #define PG8_BAR __builtin_amdgcn_s_barrier()
; #define PG8_SCHED __builtin_amdgcn_sched_barrier(0)
; #define PG8_STAGE(bufoff, gbase, voff) do { _Pragma("unroll") for (int _i = 0; _i < 2; ++_i) \
;         __builtin_amdgcn_global_load_lds((const unsigned*)((const char*)(gbase) + (voff)[_i]), (PG8_LAS unsigned*)(lds + (bufoff) + ldsw + _i * 8192), 16, 0, 0); } while (0)
; #define PG8_WAIT_V(n) asm volatile("s_waitcnt vmcnt(" #n ")" ::: "memory")
; #define PG8_WAIT_L(n) asm volatile("s_waitcnt lgkmcnt(" #n ")" ::: "memory")
; template <class Epi, class Sched, bool ALIGN_EPI = false, bool SP2 = false>
; __device__ __forceinline__ void gemm_phase(PG8_LAS unsigned char* lds, const Gemm g, const Sched& S, const Epi& E, const int tid) {
;     ...
;             PG8_WAIT_V(8); PG8_WAIT_L(0); PG8_BAR; PG8_MMA(1, 0, At, B0); PG8_MMA(1, 1, At, B1); PG8_BAR; PG8_SCHED;
;             PG8_LDB(B0, 1, 0); PG8_LDB(B1, 1, 1); PG8_SCHED; PG8_LDA(At, 1, 0); PG8_STAGE(PG8_SA(0, 1), a2 + hstep, voffA);
;             PG8_WAIT_V(8); PG8_WAIT_L(0); PG8_BAR; PG8_MMA(0, 0, At, B0); PG8_MMA(0, 1, At, B1); PG8_BAR; PG8_SCHED;
	s_setprio 1
	s_waitcnt lgkmcnt(0)
	v_mfma_f32_16x16x32_bf16 v[58:61], v[172:175], v[206:209], 0
	v_mfma_f32_16x16x32_bf16 v[50:53], v[180:183], v[206:209], 0
	v_mfma_f32_16x16x32_bf16 v[42:45], v[172:175], v[214:217], 0
	v_mfma_f32_16x16x32_bf16 v[34:37], v[180:183], v[214:217], 0
	v_mfma_f32_16x16x32_bf16 v[26:29], v[172:175], v[222:225], 0
	v_mfma_f32_16x16x32_bf16 v[18:21], v[180:183], v[222:225], 0
	v_mfma_f32_16x16x32_bf16 v[10:13], v[172:175], v[244:247], 0
	v_mfma_f32_16x16x32_bf16 v[2:5], v[180:183], v[244:247], 0
	v_mfma_f32_16x16x32_bf16 v[58:61], v[176:179], v[210:213], v[58:61]
	v_mfma_f32_16x16x32_bf16 v[50:53], v[184:187], v[210:213], v[50:53]
	v_mfma_f32_16x16x32_bf16 v[42:45], v[176:179], v[218:221], v[42:45]
	v_mfma_f32_16x16x32_bf16 v[34:37], v[184:187], v[218:221], v[34:37]
	v_mfma_f32_16x16x32_bf16 v[26:29], v[176:179], v[226:229], v[26:29]
	v_mfma_f32_16x16x32_bf16 v[18:21], v[184:187], v[226:229], v[18:21]
	v_mfma_f32_16x16x32_bf16 v[10:13], v[176:179], v[248:251], v[10:13]
	v_mfma_f32_16x16x32_bf16 v[2:5], v[184:187], v[248:251], v[2:5]
	s_setprio 0
	s_setprio 1
	v_mfma_f32_16x16x32_bf16 v[62:65], v[188:191], v[206:209], 0
	v_mfma_f32_16x16x32_bf16 v[54:57], v[198:201], v[206:209], 0
	v_mfma_f32_16x16x32_bf16 v[46:49], v[188:191], v[214:217], 0
	v_mfma_f32_16x16x32_bf16 v[38:41], v[198:201], v[214:217], 0
	v_mfma_f32_16x16x32_bf16 v[30:33], v[188:191], v[222:225], 0
	v_mfma_f32_16x16x32_bf16 v[22:25], v[198:201], v[222:225], 0
	v_mfma_f32_16x16x32_bf16 v[14:17], v[188:191], v[244:247], 0
	v_mfma_f32_16x16x32_bf16 v[6:9], v[198:201], v[244:247], 0
	v_mfma_f32_16x16x32_bf16 v[62:65], v[192:195], v[210:213], v[62:65]
	v_mfma_f32_16x16x32_bf16 v[54:57], v[202:205], v[210:213], v[54:57]
	v_mfma_f32_16x16x32_bf16 v[46:49], v[192:195], v[218:221], v[46:49]
	v_mfma_f32_16x16x32_bf16 v[38:41], v[202:205], v[218:221], v[38:41]
	v_mfma_f32_16x16x32_bf16 v[30:33], v[192:195], v[226:229], v[30:33]
	v_mfma_f32_16x16x32_bf16 v[22:25], v[202:205], v[226:229], v[22:25]
	v_mfma_f32_16x16x32_bf16 v[14:17], v[192:195], v[248:251], v[14:17]
	v_mfma_f32_16x16x32_bf16 v[6:9], v[202:205], v[248:251], v[6:9]
	s_setprio 0
	s_barrier
	s_add_i32 s26, 0, 0x18000
	v_add_u32_e32 v131, s26, v156
	s_add_i32 s31, 0, 0x1c000
	ds_read_b128 v[172:175], v131
	ds_read_b128 v[176:179], v131 offset:1024
	ds_read_b128 v[180:183], v131 offset:2048
	ds_read_b128 v[184:187], v131 offset:3072
	v_add_u32_e32 v131, s31, v156
	ds_read_b128 v[188:191], v131
	ds_read_b128 v[192:195], v131 offset:1024
	ds_read_b128 v[198:201], v131 offset:2048
	ds_read_b128 v[202:205], v131 offset:3072
	s_add_u32 s36, s56, 0x80000
	s_addc_u32 s37, s57, 0
	s_mov_b32 m0, s69
	v_lshl_add_u64 v[158:159], s[36:37], 0, v[134:135]
	ds_read_b128 v[206:209], v170 offset:32768
	ds_read_b128 v[210:213], v170 offset:33792
	ds_read_b128 v[214:217], v170 offset:34816
	ds_read_b128 v[218:221], v170 offset:35840
	ds_read_b128 v[222:225], v170 offset:36864
	ds_read_b128 v[226:229], v170 offset:37888
	ds_read_b128 v[244:247], v170 offset:38912
	ds_read_b128 v[248:251], v170 offset:39936
	global_load_lds_dwordx4 v[158:159], off
	v_lshl_add_u64 v[158:159], s[36:37], 0, v[138:139]
	s_mov_b32 m0, s70
	s_nop 0
	global_load_lds_dwordx4 v[158:159], off
	s_waitcnt vmcnt(8)
	s_waitcnt lgkmcnt(0)
	s_barrier
	s_setprio 1
	s_waitcnt lgkmcnt(0)
	v_mfma_f32_16x16x32_bf16 v[122:125], v[172:175], v[206:209], v[122:125]
	v_mfma_f32_16x16x32_bf16 v[114:117], v[180:183], v[206:209], v[114:117]
	v_mfma_f32_16x16x32_bf16 v[106:109], v[172:175], v[214:217], v[106:109]
	v_mfma_f32_16x16x32_bf16 v[98:101], v[180:183], v[214:217], v[98:101]
	v_mfma_f32_16x16x32_bf16 v[90:93], v[172:175], v[222:225], v[90:93]
	v_mfma_f32_16x16x32_bf16 v[82:85], v[180:183], v[222:225], v[82:85]
	v_mfma_f32_16x16x32_bf16 v[74:77], v[172:175], v[244:247], v[74:77]
	v_mfma_f32_16x16x32_bf16 v[66:69], v[180:183], v[244:247], v[66:69]
	v_mfma_f32_16x16x32_bf16 v[122:125], v[176:179], v[210:213], v[122:125]
	v_mfma_f32_16x16x32_bf16 v[114:117], v[184:187], v[210:213], v[114:117]
	v_mfma_f32_16x16x32_bf16 v[106:109], v[176:179], v[218:221], v[106:109]
	v_mfma_f32_16x16x32_bf16 v[98:101], v[184:187], v[218:221], v[98:101]
	v_mfma_f32_16x16x32_bf16 v[90:93], v[176:179], v[226:229], v[90:93]
	v_mfma_f32_16x16x32_bf16 v[82:85], v[184:187], v[226:229], v[82:85]
	v_mfma_f32_16x16x32_bf16 v[74:77], v[176:179], v[248:251], v[74:77]
	v_mfma_f32_16x16x32_bf16 v[66:69], v[184:187], v[248:251], v[66:69]
	s_setprio 0
	s_setprio 1
	v_mfma_f32_16x16x32_bf16 v[126:129], v[188:191], v[206:209], v[126:129]
	v_mfma_f32_16x16x32_bf16 v[118:121], v[198:201], v[206:209], v[118:121]
	v_mfma_f32_16x16x32_bf16 v[110:113], v[188:191], v[214:217], v[110:113]
	v_mfma_f32_16x16x32_bf16 v[102:105], v[198:201], v[214:217], v[102:105]
	v_mfma_f32_16x16x32_bf16 v[94:97], v[188:191], v[222:225], v[94:97]
	v_mfma_f32_16x16x32_bf16 v[86:89], v[198:201], v[222:225], v[86:89]
	v_mfma_f32_16x16x32_bf16 v[78:81], v[188:191], v[244:247], v[78:81]
	v_mfma_f32_16x16x32_bf16 v[70:73], v[198:201], v[244:247], v[70:73]
	v_mfma_f32_16x16x32_bf16 v[126:129], v[192:195], v[210:213], v[126:129]
	v_mfma_f32_16x16x32_bf16 v[118:121], v[202:205], v[210:213], v[118:121]
	v_mfma_f32_16x16x32_bf16 v[110:113], v[192:195], v[218:221], v[110:113]
	v_mfma_f32_16x16x32_bf16 v[102:105], v[202:205], v[218:221], v[102:105]
	v_mfma_f32_16x16x32_bf16 v[94:97], v[192:195], v[226:229], v[94:97]
	v_mfma_f32_16x16x32_bf16 v[86:89], v[202:205], v[226:229], v[86:89]
	v_mfma_f32_16x16x32_bf16 v[78:81], v[192:195], v[248:251], v[78:81]
	v_mfma_f32_16x16x32_bf16 v[70:73], v[202:205], v[248:251], v[70:73]
	s_setprio 0
	s_barrier
; #define PG8_STAGE(bufoff, gbase, voff) do { _Pragma("unroll") for (int _i = 0; _i < 2; ++_i) \
;         __builtin_amdgcn_global_load_lds((const unsigned*)((const char*)(gbase) + (voff)[_i]), (PG8_LAS unsigned*)(lds + (bufoff) + ldsw + _i * 8192), 16, 0, 0); } while (0)
; #define PG8_LDA(dst, b, h) do { _Pragma("unroll") for (int m = 0; m < 4; ++m) _Pragma("unroll") for (int k = 0; k < 2; ++k) dst[m][k] = *(const PG8_LAS bf16x8*)(lds + PG8_SA(b, h) + aoff + m * 2048 + k * 1024); } while (0)
; #define PG8_MMA(ai, bj, At, Bt) do { __builtin_amdgcn_s_setprio(1); _Pragma("unroll") for (int m = 0; m < 4; ++m) _Pragma("unroll") for (int n = 0; n < 2; ++n) _Pragma("unroll") for (int k = 0; k < 2; ++k) \
;         acc[ai][bj][m][n] = __builtin_amdgcn_mfma_f32_16x16x32_bf16(Bt[n][k], At[m][k], acc[ai][bj][m][n], 0, 0, 0); __builtin_amdgcn_s_setprio(0); } while (0)
; #define PG8_WAIT_V(n) asm volatile("s_waitcnt vmcnt(" #n ")" ::: "memory")
; #define PG8_WAIT_L(n) asm volatile("s_waitcnt lgkmcnt(" #n ")" ::: "memory")
; #define PG8_BAR __builtin_amdgcn_s_barrier()
; #define PG8_SCHED __builtin_amdgcn_sched_barrier(0)
; #define PG8_STAGE(bufoff, gbase, voff) do { _Pragma("unroll") for (int _i = 0; _i < 2; ++_i) \
;         __builtin_amdgcn_global_load_lds((const unsigned*)((const char*)(gbase) + (voff)[_i]), (PG8_LAS unsigned*)(lds + (bufoff) + ldsw + _i * 8192), 16, 0, 0); } while (0)
; #define PG8_LDA(dst, b, h) do { _Pragma("unroll") for (int mb = 0; mb < 2; ++mb) _Pragma("unroll") for (int s = 0; s < 2; ++s) \
;         dst[mb][s] = cat8(*(const PG8_LAS bf16x8*)(lds + PG8_SA(b, h) + aoffk[s][0] + mb * 4096), *(const PG8_LAS bf16x8*)(lds + PG8_SA(b, h) + aoffk[s][1] + mb * 4096)); } while (0)
; #define PG8_WAIT_V(n) asm volatile("s_waitcnt vmcnt(" #n ")" ::: "memory")
; template <class Epi, class Sched, bool ALIGN_EPI = false, bool SP2 = false>
; __device__ __forceinline__ void gemm_phase(PG8_LAS unsigned char* lds, const Gemm g, const Sched& S, const Epi& E, const int tid) {
;     ...
;         for (int t = 0; t < nt; t += 2) {
;             const bool last = (t == nt - 2);
;     ...
;             PG8_LDA(At, 1, 1); PG8_STAGE(PG8_SB(1, 0), b3, voffB); PG8_STAGE(PG8_SB(1, 1), b3 + hstep, voffB); PG8_STAGE(PG8_SA(1, 0), a3, voffA);
;             PG8_WAIT_V(8); PG8_WAIT_L(0); PG8_BAR; PG8_MMA(1, 0, At, B0); PG8_MMA(1, 1, At, B1); PG8_BAR; PG8_SCHED;
	s_add_i32 s26, s26, s64
	v_lshl_add_u64 v[132:133], v[132:133], 0, s[34:35]
	s_mov_b32 m0, s26
	ds_read_b128 v[206:209], v170 offset:49152
	ds_read_b128 v[210:213], v170 offset:50176
	ds_read_b128 v[214:217], v170 offset:51200
	ds_read_b128 v[218:221], v170 offset:52224
	ds_read_b128 v[222:225], v170 offset:53248
	ds_read_b128 v[226:229], v170 offset:54272
	ds_read_b128 v[244:247], v170 offset:55296
	ds_read_b128 v[248:251], v170 offset:56320
	global_load_lds_dwordx4 v[132:133], off
	s_add_i32 m0, s26, 0x2000
	s_add_u32 s6, s6, 0x80080
	v_lshl_add_u64 v[132:133], v[152:153], 0, s[34:35]
	s_addc_u32 s7, s7, 0
	s_add_i32 s26, s31, s64
	global_load_lds_dwordx4 v[132:133], off
	v_lshl_add_u64 v[132:133], s[6:7], 0, v[136:137]
	s_mov_b32 m0, s26
	s_nop 0
	global_load_lds_dwordx4 v[132:133], off
	v_lshl_add_u64 v[132:133], s[6:7], 0, v[140:141]
	s_add_i32 m0, s26, 0x2000
	s_nop 0
	global_load_lds_dwordx4 v[132:133], off
	v_lshl_add_u64 v[132:133], v[230:231], 0, s[34:35]
	s_mov_b32 m0, s72
	s_nop 0
	global_load_lds_dwordx4 v[132:133], off
	v_lshl_add_u64 v[132:133], v[242:243], 0, s[34:35]
	s_mov_b32 m0, s73
	s_nop 0
	global_load_lds_dwordx4 v[132:133], off
	s_waitcnt vmcnt(8)
	s_waitcnt lgkmcnt(0)
	s_barrier
	s_setprio 1
	s_waitcnt lgkmcnt(0)
	v_mfma_f32_16x16x32_bf16 v[58:61], v[172:175], v[206:209], v[58:61]
	v_mfma_f32_16x16x32_bf16 v[50:53], v[180:183], v[206:209], v[50:53]
	v_mfma_f32_16x16x32_bf16 v[42:45], v[172:175], v[214:217], v[42:45]
	v_mfma_f32_16x16x32_bf16 v[34:37], v[180:183], v[214:217], v[34:37]
	v_mfma_f32_16x16x32_bf16 v[26:29], v[172:175], v[222:225], v[26:29]
	v_mfma_f32_16x16x32_bf16 v[18:21], v[180:183], v[222:225], v[18:21]
	v_mfma_f32_16x16x32_bf16 v[10:13], v[172:175], v[244:247], v[10:13]
	v_mfma_f32_16x16x32_bf16 v[2:5], v[180:183], v[244:247], v[2:5]
	v_mfma_f32_16x16x32_bf16 v[58:61], v[176:179], v[210:213], v[58:61]
	v_mfma_f32_16x16x32_bf16 v[50:53], v[184:187], v[210:213], v[50:53]
	v_mfma_f32_16x16x32_bf16 v[42:45], v[176:179], v[218:221], v[42:45]
	v_mfma_f32_16x16x32_bf16 v[34:37], v[184:187], v[218:221], v[34:37]
	v_mfma_f32_16x16x32_bf16 v[26:29], v[176:179], v[226:229], v[26:29]
	v_mfma_f32_16x16x32_bf16 v[18:21], v[184:187], v[226:229], v[18:21]
	v_mfma_f32_16x16x32_bf16 v[10:13], v[176:179], v[248:251], v[10:13]
	v_mfma_f32_16x16x32_bf16 v[2:5], v[184:187], v[248:251], v[2:5]
	s_setprio 0
	s_setprio 1
	v_mfma_f32_16x16x32_bf16 v[62:65], v[188:191], v[206:209], v[62:65]
	v_mfma_f32_16x16x32_bf16 v[54:57], v[198:201], v[206:209], v[54:57]
	v_mfma_f32_16x16x32_bf16 v[46:49], v[188:191], v[214:217], v[46:49]
	v_mfma_f32_16x16x32_bf16 v[38:41], v[198:201], v[214:217], v[38:41]
	v_mfma_f32_16x16x32_bf16 v[30:33], v[188:191], v[222:225], v[30:33]
	v_mfma_f32_16x16x32_bf16 v[22:25], v[198:201], v[222:225], v[22:25]
	v_mfma_f32_16x16x32_bf16 v[14:17], v[188:191], v[244:247], v[14:17]
	v_mfma_f32_16x16x32_bf16 v[6:9], v[198:201], v[244:247], v[6:9]
	v_mfma_f32_16x16x32_bf16 v[62:65], v[192:195], v[210:213], v[62:65]
	v_mfma_f32_16x16x32_bf16 v[54:57], v[202:205], v[210:213], v[54:57]
	v_mfma_f32_16x16x32_bf16 v[46:49], v[192:195], v[218:221], v[46:49]
	v_mfma_f32_16x16x32_bf16 v[38:41], v[202:205], v[218:221], v[38:41]
	v_mfma_f32_16x16x32_bf16 v[30:33], v[192:195], v[226:229], v[30:33]
	v_mfma_f32_16x16x32_bf16 v[22:25], v[202:205], v[226:229], v[22:25]
	v_mfma_f32_16x16x32_bf16 v[14:17], v[192:195], v[248:251], v[14:17]
	v_mfma_f32_16x16x32_bf16 v[6:9], v[202:205], v[248:251], v[6:9]
	s_setprio 0
	s_barrier
	s_add_i32 s24, s24, 2
	s_add_u32 s54, s54, 0x100
	s_addc_u32 s55, s55, 0
	s_add_u32 s18, s18, 0x100
	s_addc_u32 s19, s19, 0
	s_cmp_gt_u32 s24, 29
	s_cbranch_scc1 .Lpeel_exit_2282

; #define PG8_BAR __builtin_amdgcn_s_barrier()
; #define PG8_BAR __builtin_amdgcn_s_barrier()
; template <class Epi, class Sched, bool ALIGN_EPI = false, bool SP2 = false>
; __device__ __forceinline__ void gemm_phase(PG8_LAS unsigned char* lds, const Gemm g, const Sched& S, const Epi& E, const int tid) {
;     ...
;         if constexpr (ALIGN_EPI) { if (wr == 0) PG8_BAR; }
.Lpeel_exit_2282:
	s_and_b64 vcc, exec, s[10:11]
	s_cbranch_vccz .LBB0_2285
	s_barrier

; #define PG8_STAGE(bufoff, gbase, voff) do { _Pragma("unroll") for (int _i = 0; _i < 2; ++_i) \
;         __builtin_amdgcn_global_load_lds((const unsigned*)((const char*)(gbase) + (voff)[_i]), (PG8_LAS unsigned*)(lds + (bufoff) + ldsw + _i * 8192), 16, 0, 0); } while (0)
; #define PG8_LDA(dst, b, h) do { _Pragma("unroll") for (int m = 0; m < 4; ++m) _Pragma("unroll") for (int k = 0; k < 2; ++k) dst[m][k] = *(const PG8_LAS bf16x8*)(lds + PG8_SA(b, h) + aoff + m * 2048 + k * 1024); } while (0)
; #define PG8_LDB(dst, b, h) do { _Pragma("unroll") for (int n = 0; n < 2; ++n) _Pragma("unroll") for (int k = 0; k < 2; ++k) dst[n][k] = *(const PG8_LAS bf16x8*)(lds + PG8_SB(b, h) + boff + n * 2048 + k * 1024); } while (0)
; #define PG8_WAIT_V(n) asm volatile("s_waitcnt vmcnt(" #n ")" ::: "memory")
; #define PG8_WAIT_L(n) asm volatile("s_waitcnt lgkmcnt(" #n ")" ::: "memory")
; #define PG8_BAR __builtin_amdgcn_s_barrier()
; #define PG8_SCHED __builtin_amdgcn_sched_barrier(0)
; #define PG8_WAIT_V(n) asm volatile("s_waitcnt vmcnt(" #n ")" ::: "memory")
; template <class Epi, class Sched, bool ALIGN_EPI = false, bool SP2 = false>
; __device__ __forceinline__ void gemm_phase(PG8_LAS unsigned char* lds, const Gemm g, const Sched& S, const Epi& E, const int tid) {
;     ...
;         const bool has_next = S.next(ui + 1, nxt);
;         const char* nA = has_next ? (const char*)g.A + (size_t)nxt.pm * tstep + (size_t)nxt.k0 * 2 : cA; const char* nB = has_next ? (const char*)g.Bt + (size_t)nxt.pn * tstep + (size_t)nxt.k0 * 2 : cB;
;         for (int t = 0; t < nt; t += 2) {
;             const bool last = (t == nt - 2);
;             const char* a1 = cA + (size_t)(t + 1) * kstep;
;             const char* a2 = last ? nA : cA + (size_t)(t + 2) * kstep; const char* b2 = last ? nB : cB + (size_t)(t + 2) * kstep;
;             const char* a3 = a2 + kstep; const char* b3 = b2 + kstep;
;             if (last && has_next) S.a_ready(nxt);
;             if constexpr (SP2) {
;             PG8_LDB(B0, 0, 0); PG8_LDB(B1, 0, 1); PG8_SCHED; PG8_LDA(At, 0, 0); PG8_STAGE(PG8_SA(1, 1), a1 + hstep, voffA);
;             PG8_WAIT_V(8); PG8_WAIT_L(0); PG8_BAR; PG8_MMA(0, 0, At, B0); PG8_MMA(0, 1, At, B1); PG8_BAR; PG8_SCHED;
;             PG8_LDA(At, 0, 1); PG8_STAGE(PG8_SB(0, 0), b2, voffB); PG8_STAGE(PG8_SB(0, 1), b2 + hstep, voffB); PG8_STAGE(PG8_SA(0, 0), a2, voffA);
.LBB0_2524:
	s_add_i32 s12, s2, -2
	s_add_u32 s13, s6, 0x100
	v_mov_b32_e32 v2, 0
	s_addc_u32 s15, s7, 0
	s_mov_b32 s18, 0
	s_add_i32 s19, s18, 2
	s_add_u32 s6, s22, 0x100
	s_addc_u32 s7, s23, 0
	s_add_i32 s26, 0, 0x10000
	s_cmp_eq_u32 s12, s18
	s_cselect_b32 s31, s17, s7
	s_cselect_b32 s30, s16, s6
	s_cselect_b32 s29, s21, s15
	s_cselect_b32 s28, s20, s13
	s_add_i32 s18, 0, 0x14000
	v_add_u32_e32 v144, s26, v162
	v_add_u32_e32 v160, s18, v162
	ds_read_b128 v[132:135], v144
	ds_read_b128 v[136:139], v144 offset:1024
	ds_read_b128 v[140:143], v144 offset:2048
	ds_read_b128 v[144:147], v144 offset:3072
	ds_read_b128 v[172:175], v160
	ds_read_b128 v[176:179], v160 offset:1024
	ds_read_b128 v[180:183], v160 offset:2048
	ds_read_b128 v[184:187], v160 offset:3072
	v_lshl_add_u64 v[160:161], s[22:23], 0, v[156:157]
	s_add_i32 m0, s44, 0xc000
	ds_read_b128 v[188:191], v171
	ds_read_b128 v[192:195], v171 offset:1024
	ds_read_b128 v[198:201], v171 offset:2048
	ds_read_b128 v[202:205], v171 offset:3072
	ds_read_b128 v[206:209], v171 offset:4096
	ds_read_b128 v[210:213], v171 offset:5120
	ds_read_b128 v[214:217], v171 offset:6144
	ds_read_b128 v[218:221], v171 offset:7168
	global_load_lds_dwordx4 v[160:161], off
	v_lshl_add_u64 v[160:161], s[22:23], 0, v[158:159]
	s_add_i32 m0, s44, 0xe000
	s_nop 0
	global_load_lds_dwordx4 v[160:161], off
	s_waitcnt vmcnt(8)
	s_waitcnt lgkmcnt(0)
	s_barrier
	s_setprio 1
	s_waitcnt lgkmcnt(0)
	v_mfma_f32_16x16x32_bf16 v[126:129], v[132:135], v[188:191], 0
	v_mfma_f32_16x16x32_bf16 v[122:125], v[140:143], v[188:191], 0
	v_mfma_f32_16x16x32_bf16 v[114:117], v[132:135], v[198:201], 0
	v_mfma_f32_16x16x32_bf16 v[106:109], v[140:143], v[198:201], 0
	v_mfma_f32_16x16x32_bf16 v[98:101], v[132:135], v[206:209], 0
	v_mfma_f32_16x16x32_bf16 v[90:93], v[140:143], v[206:209], 0
	v_mfma_f32_16x16x32_bf16 v[82:85], v[132:135], v[214:217], 0
	v_mfma_f32_16x16x32_bf16 v[74:77], v[140:143], v[214:217], 0
	v_mfma_f32_16x16x32_bf16 v[126:129], v[136:139], v[192:195], v[126:129]
	v_mfma_f32_16x16x32_bf16 v[122:125], v[144:147], v[192:195], v[122:125]
	v_mfma_f32_16x16x32_bf16 v[114:117], v[136:139], v[202:205], v[114:117]
	v_mfma_f32_16x16x32_bf16 v[106:109], v[144:147], v[202:205], v[106:109]
	v_mfma_f32_16x16x32_bf16 v[98:101], v[136:139], v[210:213], v[98:101]
	v_mfma_f32_16x16x32_bf16 v[90:93], v[144:147], v[210:213], v[90:93]
	v_mfma_f32_16x16x32_bf16 v[82:85], v[136:139], v[218:221], v[82:85]
	v_mfma_f32_16x16x32_bf16 v[74:77], v[144:147], v[218:221], v[74:77]
	s_setprio 0
	s_setprio 1
	v_mfma_f32_16x16x32_bf16 v[118:121], v[172:175], v[188:191], 0
	v_mfma_f32_16x16x32_bf16 v[110:113], v[180:183], v[188:191], 0
	v_mfma_f32_16x16x32_bf16 v[102:105], v[172:175], v[198:201], 0
	v_mfma_f32_16x16x32_bf16 v[94:97], v[180:183], v[198:201], 0
	v_mfma_f32_16x16x32_bf16 v[86:89], v[172:175], v[206:209], 0
	v_mfma_f32_16x16x32_bf16 v[78:81], v[180:183], v[206:209], 0
	v_mfma_f32_16x16x32_bf16 v[70:73], v[172:175], v[214:217], 0
	v_mfma_f32_16x16x32_bf16 v[66:69], v[180:183], v[214:217], 0
	v_mfma_f32_16x16x32_bf16 v[118:121], v[176:179], v[192:195], v[118:121]
	v_mfma_f32_16x16x32_bf16 v[110:113], v[184:187], v[192:195], v[110:113]
	v_mfma_f32_16x16x32_bf16 v[102:105], v[176:179], v[202:205], v[102:105]
	v_mfma_f32_16x16x32_bf16 v[94:97], v[184:187], v[202:205], v[94:97]
	v_mfma_f32_16x16x32_bf16 v[86:89], v[176:179], v[210:213], v[86:89]
	v_mfma_f32_16x16x32_bf16 v[78:81], v[184:187], v[210:213], v[78:81]
	v_mfma_f32_16x16x32_bf16 v[70:73], v[176:179], v[218:221], v[70:73]
	v_mfma_f32_16x16x32_bf16 v[66:69], v[184:187], v[218:221], v[66:69]
	s_setprio 0
	s_barrier
	s_add_i32 s22, s26, s43
	v_lshl_add_u64 v[160:161], s[28:29], 0, v[150:151]
	s_mov_b32 m0, s22
	ds_read_b128 v[188:191], v171 offset:16384
	ds_read_b128 v[192:195], v171 offset:17408
	ds_read_b128 v[198:201], v171 offset:18432
	ds_read_b128 v[202:205], v171 offset:19456
	ds_read_b128 v[206:209], v171 offset:20480
	ds_read_b128 v[210:213], v171 offset:21504
	ds_read_b128 v[214:217], v171 offset:22528
	ds_read_b128 v[218:221], v171 offset:23552
	global_load_lds_dwordx4 v[160:161], off
	s_add_i32 m0, s22, 0x2000
	s_add_u32 s22, s28, 0x160000
	v_lshl_add_u64 v[222:223], s[28:29], 0, v[154:155]
	s_addc_u32 s23, s29, 0
	s_add_i32 s18, s18, s43
	global_load_lds_dwordx4 v[222:223], off
	v_lshl_add_u64 v[224:225], s[22:23], 0, v[150:151]
	s_mov_b32 m0, s18
	v_lshl_add_u64 v[226:227], s[30:31], 0, v[152:153]
	global_load_lds_dwordx4 v[224:225], off
	v_lshl_add_u64 v[224:225], s[22:23], 0, v[154:155]
	s_add_i32 m0, s18, 0x2000
	s_nop 0
	global_load_lds_dwordx4 v[224:225], off
	v_lshl_add_u64 v[224:225], s[30:31], 0, v[148:149]
	s_mov_b32 m0, s44
	s_nop 0
	global_load_lds_dwordx4 v[224:225], off
	s_mov_b32 m0, s45
	s_nop 0
	global_load_lds_dwordx4 v[226:227], off
	s_waitcnt vmcnt(8)
	s_waitcnt lgkmcnt(0)
	s_barrier
; #define PG8_STAGE(bufoff, gbase, voff) do { _Pragma("unroll") for (int _i = 0; _i < 2; ++_i) \
;         __builtin_amdgcn_global_load_lds((const unsigned*)((const char*)(gbase) + (voff)[_i]), (PG8_LAS unsigned*)(lds + (bufoff) + ldsw + _i * 8192), 16, 0, 0); } while (0)
; #define PG8_LDA(dst, b, h) do { _Pragma("unroll") for (int m = 0; m < 4; ++m) _Pragma("unroll") for (int k = 0; k < 2; ++k) dst[m][k] = *(const PG8_LAS bf16x8*)(lds + PG8_SA(b, h) + aoff + m * 2048 + k * 1024); } while (0)
; #define PG8_LDB(dst, b, h) do { _Pragma("unroll") for (int n = 0; n < 2; ++n) _Pragma("unroll") for (int k = 0; k < 2; ++k) dst[n][k] = *(const PG8_LAS bf16x8*)(lds + PG8_SB(b, h) + boff + n * 2048 + k * 1024); } while (0)
; #define PG8_MMA(ai, bj, At, Bt) do { __builtin_amdgcn_s_setprio(1); _Pragma("unroll") for (int m = 0; m < 4; ++m) _Pragma("unroll") for (int n = 0; n < 2; ++n) _Pragma("unroll") for (int k = 0; k < 2; ++k) \
;         acc[ai][bj][m][n] = __builtin_amdgcn_mfma_f32_16x16x32_bf16(Bt[n][k], At[m][k], acc[ai][bj][m][n], 0, 0, 0); __builtin_amdgcn_s_setprio(0); } while (0)
; #define PG8_WAIT_V(n) asm volatile("s_waitcnt vmcnt(" #n ")" ::: "memory")
; #define PG8_WAIT_L(n) asm volatile("s_waitcnt lgkmcnt(" #n ")" ::: "memory")
; #define PG8_BAR __builtin_amdgcn_s_barrier()
; #define PG8_SCHED __builtin_amdgcn_sched_barrier(0)
; #define PG8_STAGE(bufoff, gbase, voff) do { _Pragma("unroll") for (int _i = 0; _i < 2; ++_i) \
;         __builtin_amdgcn_global_load_lds((const unsigned*)((const char*)(gbase) + (voff)[_i]), (PG8_LAS unsigned*)(lds + (bufoff) + ldsw + _i * 8192), 16, 0, 0); } while (0)
; #define PG8_WAIT_V(n) asm volatile("s_waitcnt vmcnt(" #n ")" ::: "memory")
; #define PG8_WAIT_L(n) asm volatile("s_waitcnt lgkmcnt(" #n ")" ::: "memory")
; template <class Epi, class Sched, bool ALIGN_EPI = false, bool SP2 = false>
; __device__ __forceinline__ void gemm_phase(PG8_LAS unsigned char* lds, const Gemm g, const Sched& S, const Epi& E, const int tid) {
;     ...
;             PG8_WAIT_V(8); PG8_WAIT_L(0); PG8_BAR; PG8_MMA(1, 0, At, B0); PG8_MMA(1, 1, At, B1); PG8_BAR; PG8_SCHED;
;             PG8_LDB(B0, 1, 0); PG8_LDB(B1, 1, 1); PG8_SCHED; PG8_LDA(At, 1, 0); PG8_STAGE(PG8_SA(0, 1), a2 + hstep, voffA);
;             PG8_WAIT_V(8); PG8_WAIT_L(0); PG8_BAR; PG8_MMA(0, 0, At, B0); PG8_MMA(0, 1, At, B1); PG8_BAR; PG8_SCHED;
	s_setprio 1
	s_waitcnt lgkmcnt(0)
	v_mfma_f32_16x16x32_bf16 v[62:65], v[132:135], v[188:191], 0
	v_mfma_f32_16x16x32_bf16 v[58:61], v[140:143], v[188:191], 0
	v_mfma_f32_16x16x32_bf16 v[50:53], v[132:135], v[198:201], 0
	v_mfma_f32_16x16x32_bf16 v[42:45], v[140:143], v[198:201], 0
	v_mfma_f32_16x16x32_bf16 v[34:37], v[132:135], v[206:209], 0
	v_mfma_f32_16x16x32_bf16 v[26:29], v[140:143], v[206:209], 0
	v_mfma_f32_16x16x32_bf16 v[18:21], v[132:135], v[214:217], 0
	v_mfma_f32_16x16x32_bf16 v[10:13], v[140:143], v[214:217], 0
	v_mfma_f32_16x16x32_bf16 v[62:65], v[136:139], v[192:195], v[62:65]
	v_mfma_f32_16x16x32_bf16 v[58:61], v[144:147], v[192:195], v[58:61]
	v_mfma_f32_16x16x32_bf16 v[50:53], v[136:139], v[202:205], v[50:53]
	v_mfma_f32_16x16x32_bf16 v[42:45], v[144:147], v[202:205], v[42:45]
	v_mfma_f32_16x16x32_bf16 v[34:37], v[136:139], v[210:213], v[34:37]
	v_mfma_f32_16x16x32_bf16 v[26:29], v[144:147], v[210:213], v[26:29]
	v_mfma_f32_16x16x32_bf16 v[18:21], v[136:139], v[218:221], v[18:21]
	v_mfma_f32_16x16x32_bf16 v[10:13], v[144:147], v[218:221], v[10:13]
	s_setprio 0
	s_setprio 1
	v_mfma_f32_16x16x32_bf16 v[54:57], v[172:175], v[188:191], 0
	v_mfma_f32_16x16x32_bf16 v[46:49], v[180:183], v[188:191], 0
	v_mfma_f32_16x16x32_bf16 v[38:41], v[172:175], v[198:201], 0
	v_mfma_f32_16x16x32_bf16 v[30:33], v[180:183], v[198:201], 0
	v_mfma_f32_16x16x32_bf16 v[22:25], v[172:175], v[206:209], 0
	v_mfma_f32_16x16x32_bf16 v[14:17], v[180:183], v[206:209], 0
	v_mfma_f32_16x16x32_bf16 v[6:9], v[172:175], v[214:217], 0
	v_mfma_f32_16x16x32_bf16 v[2:5], v[180:183], v[214:217], 0
	v_mfma_f32_16x16x32_bf16 v[54:57], v[176:179], v[192:195], v[54:57]
	v_mfma_f32_16x16x32_bf16 v[46:49], v[184:187], v[192:195], v[46:49]
	v_mfma_f32_16x16x32_bf16 v[38:41], v[176:179], v[202:205], v[38:41]
	v_mfma_f32_16x16x32_bf16 v[30:33], v[184:187], v[202:205], v[30:33]
	v_mfma_f32_16x16x32_bf16 v[22:25], v[176:179], v[210:213], v[22:25]
	v_mfma_f32_16x16x32_bf16 v[14:17], v[184:187], v[210:213], v[14:17]
	v_mfma_f32_16x16x32_bf16 v[6:9], v[176:179], v[218:221], v[6:9]
	v_mfma_f32_16x16x32_bf16 v[2:5], v[184:187], v[218:221], v[2:5]
	s_setprio 0
	s_barrier
	s_add_i32 s18, 0, 0x18000
	s_add_i32 s26, 0, 0x1c000
	v_add_u32_e32 v144, s18, v162
	v_add_u32_e32 v184, s26, v162
	ds_read_b128 v[132:135], v144
	ds_read_b128 v[136:139], v144 offset:1024
	ds_read_b128 v[140:143], v144 offset:2048
	ds_read_b128 v[144:147], v144 offset:3072
	ds_read_b128 v[172:175], v184
	ds_read_b128 v[176:179], v184 offset:1024
	ds_read_b128 v[180:183], v184 offset:2048
	ds_read_b128 v[184:187], v184 offset:3072
	s_add_u32 s22, s30, 0x160000
	s_addc_u32 s23, s31, 0
	s_mov_b32 m0, s46
	v_lshl_add_u64 v[228:229], s[22:23], 0, v[148:149]
	ds_read_b128 v[188:191], v171 offset:32768
	ds_read_b128 v[192:195], v171 offset:33792
	ds_read_b128 v[198:201], v171 offset:34816
	ds_read_b128 v[202:205], v171 offset:35840
	ds_read_b128 v[206:209], v171 offset:36864
	ds_read_b128 v[210:213], v171 offset:37888
	ds_read_b128 v[214:217], v171 offset:38912
	ds_read_b128 v[218:221], v171 offset:39936
	global_load_lds_dwordx4 v[228:229], off
	v_lshl_add_u64 v[228:229], s[22:23], 0, v[152:153]
	s_mov_b32 m0, s47
	s_nop 0
	global_load_lds_dwordx4 v[228:229], off
	s_waitcnt vmcnt(8)
	s_waitcnt lgkmcnt(0)
	s_barrier
	s_setprio 1
	s_waitcnt lgkmcnt(0)
	v_mfma_f32_16x16x32_bf16 v[126:129], v[132:135], v[188:191], v[126:129]
	v_mfma_f32_16x16x32_bf16 v[122:125], v[140:143], v[188:191], v[122:125]
	v_mfma_f32_16x16x32_bf16 v[114:117], v[132:135], v[198:201], v[114:117]
	v_mfma_f32_16x16x32_bf16 v[106:109], v[140:143], v[198:201], v[106:109]
	v_mfma_f32_16x16x32_bf16 v[98:101], v[132:135], v[206:209], v[98:101]
	v_mfma_f32_16x16x32_bf16 v[90:93], v[140:143], v[206:209], v[90:93]
	v_mfma_f32_16x16x32_bf16 v[82:85], v[132:135], v[214:217], v[82:85]
	v_mfma_f32_16x16x32_bf16 v[74:77], v[140:143], v[214:217], v[74:77]
	v_mfma_f32_16x16x32_bf16 v[126:129], v[136:139], v[192:195], v[126:129]
	v_mfma_f32_16x16x32_bf16 v[122:125], v[144:147], v[192:195], v[122:125]
	v_mfma_f32_16x16x32_bf16 v[114:117], v[136:139], v[202:205], v[114:117]
	v_mfma_f32_16x16x32_bf16 v[106:109], v[144:147], v[202:205], v[106:109]
	v_mfma_f32_16x16x32_bf16 v[98:101], v[136:139], v[210:213], v[98:101]
	v_mfma_f32_16x16x32_bf16 v[90:93], v[144:147], v[210:213], v[90:93]
	v_mfma_f32_16x16x32_bf16 v[82:85], v[136:139], v[218:221], v[82:85]
	v_mfma_f32_16x16x32_bf16 v[74:77], v[144:147], v[218:221], v[74:77]
	s_setprio 0
	s_setprio 1
	v_mfma_f32_16x16x32_bf16 v[118:121], v[172:175], v[188:191], v[118:121]
	v_mfma_f32_16x16x32_bf16 v[110:113], v[180:183], v[188:191], v[110:113]
	v_mfma_f32_16x16x32_bf16 v[102:105], v[172:175], v[198:201], v[102:105]
	v_mfma_f32_16x16x32_bf16 v[94:97], v[180:183], v[198:201], v[94:97]
	v_mfma_f32_16x16x32_bf16 v[86:89], v[172:175], v[206:209], v[86:89]
	v_mfma_f32_16x16x32_bf16 v[78:81], v[180:183], v[206:209], v[78:81]
	v_mfma_f32_16x16x32_bf16 v[70:73], v[172:175], v[214:217], v[70:73]
	v_mfma_f32_16x16x32_bf16 v[66:69], v[180:183], v[214:217], v[66:69]
	v_mfma_f32_16x16x32_bf16 v[118:121], v[176:179], v[192:195], v[118:121]
	v_mfma_f32_16x16x32_bf16 v[110:113], v[184:187], v[192:195], v[110:113]
	v_mfma_f32_16x16x32_bf16 v[102:105], v[176:179], v[202:205], v[102:105]
	v_mfma_f32_16x16x32_bf16 v[94:97], v[184:187], v[202:205], v[94:97]
	v_mfma_f32_16x16x32_bf16 v[86:89], v[176:179], v[210:213], v[86:89]
	v_mfma_f32_16x16x32_bf16 v[78:81], v[184:187], v[210:213], v[78:81]
	v_mfma_f32_16x16x32_bf16 v[70:73], v[176:179], v[218:221], v[70:73]
	v_mfma_f32_16x16x32_bf16 v[66:69], v[184:187], v[218:221], v[66:69]
	s_setprio 0
	s_barrier
; #define PG8_STAGE(bufoff, gbase, voff) do { _Pragma("unroll") for (int _i = 0; _i < 2; ++_i) \
;         __builtin_amdgcn_global_load_lds((const unsigned*)((const char*)(gbase) + (voff)[_i]), (PG8_LAS unsigned*)(lds + (bufoff) + ldsw + _i * 8192), 16, 0, 0); } while (0)
; #define PG8_LDA(dst, b, h) do { _Pragma("unroll") for (int m = 0; m < 4; ++m) _Pragma("unroll") for (int k = 0; k < 2; ++k) dst[m][k] = *(const PG8_LAS bf16x8*)(lds + PG8_SA(b, h) + aoff + m * 2048 + k * 1024); } while (0)
; #define PG8_MMA(ai, bj, At, Bt) do { __builtin_amdgcn_s_setprio(1); _Pragma("unroll") for (int m = 0; m < 4; ++m) _Pragma("unroll") for (int n = 0; n < 2; ++n) _Pragma("unroll") for (int k = 0; k < 2; ++k) \
;         acc[ai][bj][m][n] = __builtin_amdgcn_mfma_f32_16x16x32_bf16(Bt[n][k], At[m][k], acc[ai][bj][m][n], 0, 0, 0); __builtin_amdgcn_s_setprio(0); } while (0)
; #define PG8_WAIT_V(n) asm volatile("s_waitcnt vmcnt(" #n ")" ::: "memory")
; #define PG8_WAIT_L(n) asm volatile("s_waitcnt lgkmcnt(" #n ")" ::: "memory")
; #define PG8_BAR __builtin_amdgcn_s_barrier()
; #define PG8_SCHED __builtin_amdgcn_sched_barrier(0)
; #define PG8_STAGE(bufoff, gbase, voff) do { _Pragma("unroll") for (int _i = 0; _i < 2; ++_i) \
;         __builtin_amdgcn_global_load_lds((const unsigned*)((const char*)(gbase) + (voff)[_i]), (PG8_LAS unsigned*)(lds + (bufoff) + ldsw + _i * 8192), 16, 0, 0); } while (0)
; #define PG8_LDA(dst, b, h) do { _Pragma("unroll") for (int mb = 0; mb < 2; ++mb) _Pragma("unroll") for (int s = 0; s < 2; ++s) \
;         dst[mb][s] = cat8(*(const PG8_LAS bf16x8*)(lds + PG8_SA(b, h) + aoffk[s][0] + mb * 4096), *(const PG8_LAS bf16x8*)(lds + PG8_SA(b, h) + aoffk[s][1] + mb * 4096)); } while (0)
; #define PG8_WAIT_V(n) asm volatile("s_waitcnt vmcnt(" #n ")" ::: "memory")
; template <class Epi, class Sched, bool ALIGN_EPI = false, bool SP2 = false>
; __device__ __forceinline__ void gemm_phase(PG8_LAS unsigned char* lds, const Gemm g, const Sched& S, const Epi& E, const int tid) {
;     ...
;         for (int t = 0; t < nt; t += 2) {
;             const bool last = (t == nt - 2);
;     ...
;             PG8_LDA(At, 1, 1); PG8_STAGE(PG8_SB(1, 0), b3, voffB); PG8_STAGE(PG8_SB(1, 1), b3 + hstep, voffB); PG8_STAGE(PG8_SA(1, 0), a3, voffA);
;             PG8_WAIT_V(8); PG8_WAIT_L(0); PG8_BAR; PG8_MMA(1, 0, At, B0); PG8_MMA(1, 1, At, B1); PG8_BAR; PG8_SCHED;
	s_add_i32 s18, s18, s43
	v_lshl_add_u64 v[160:161], v[160:161], 0, s[34:35]
	s_mov_b32 m0, s18
	ds_read_b128 v[188:191], v171 offset:49152
	ds_read_b128 v[192:195], v171 offset:50176
	ds_read_b128 v[198:201], v171 offset:51200
	ds_read_b128 v[202:205], v171 offset:52224
	ds_read_b128 v[206:209], v171 offset:53248
	ds_read_b128 v[210:213], v171 offset:54272
	ds_read_b128 v[214:217], v171 offset:55296
	ds_read_b128 v[218:221], v171 offset:56320
	global_load_lds_dwordx4 v[160:161], off
	s_add_i32 m0, s18, 0x2000
	s_add_u32 s22, s28, 0x160080
	v_lshl_add_u64 v[160:161], v[222:223], 0, s[34:35]
	s_addc_u32 s23, s29, 0
	s_add_i32 s18, s26, s43
	global_load_lds_dwordx4 v[160:161], off
	v_lshl_add_u64 v[160:161], s[22:23], 0, v[150:151]
	s_mov_b32 m0, s18
	s_nop 0
	global_load_lds_dwordx4 v[160:161], off
	v_lshl_add_u64 v[160:161], s[22:23], 0, v[154:155]
	s_add_i32 m0, s18, 0x2000
	s_nop 0
	global_load_lds_dwordx4 v[160:161], off
	v_lshl_add_u64 v[160:161], v[224:225], 0, s[34:35]
	s_mov_b32 m0, s48
	s_nop 0
	global_load_lds_dwordx4 v[160:161], off
	v_lshl_add_u64 v[160:161], v[226:227], 0, s[34:35]
	s_mov_b32 m0, s49
	s_nop 0
	global_load_lds_dwordx4 v[160:161], off
	s_waitcnt vmcnt(8)
	s_waitcnt lgkmcnt(0)
	s_barrier
	s_setprio 1
	s_waitcnt lgkmcnt(0)
	v_mfma_f32_16x16x32_bf16 v[62:65], v[132:135], v[188:191], v[62:65]
	v_mfma_f32_16x16x32_bf16 v[58:61], v[140:143], v[188:191], v[58:61]
	v_mfma_f32_16x16x32_bf16 v[50:53], v[132:135], v[198:201], v[50:53]
	v_mfma_f32_16x16x32_bf16 v[42:45], v[140:143], v[198:201], v[42:45]
	v_mfma_f32_16x16x32_bf16 v[34:37], v[132:135], v[206:209], v[34:37]
	v_mfma_f32_16x16x32_bf16 v[26:29], v[140:143], v[206:209], v[26:29]
	v_mfma_f32_16x16x32_bf16 v[18:21], v[132:135], v[214:217], v[18:21]
	v_mfma_f32_16x16x32_bf16 v[10:13], v[140:143], v[214:217], v[10:13]
	v_mfma_f32_16x16x32_bf16 v[62:65], v[136:139], v[192:195], v[62:65]
	v_mfma_f32_16x16x32_bf16 v[58:61], v[144:147], v[192:195], v[58:61]
	v_mfma_f32_16x16x32_bf16 v[50:53], v[136:139], v[202:205], v[50:53]
	v_mfma_f32_16x16x32_bf16 v[42:45], v[144:147], v[202:205], v[42:45]
	v_mfma_f32_16x16x32_bf16 v[34:37], v[136:139], v[210:213], v[34:37]
	v_mfma_f32_16x16x32_bf16 v[26:29], v[144:147], v[210:213], v[26:29]
	v_mfma_f32_16x16x32_bf16 v[18:21], v[136:139], v[218:221], v[18:21]
	v_mfma_f32_16x16x32_bf16 v[10:13], v[144:147], v[218:221], v[10:13]
	s_setprio 0
	s_setprio 1
	v_mfma_f32_16x16x32_bf16 v[54:57], v[172:175], v[188:191], v[54:57]
	v_mfma_f32_16x16x32_bf16 v[46:49], v[180:183], v[188:191], v[46:49]
	v_mfma_f32_16x16x32_bf16 v[38:41], v[172:175], v[198:201], v[38:41]
	v_mfma_f32_16x16x32_bf16 v[30:33], v[180:183], v[198:201], v[30:33]
	v_mfma_f32_16x16x32_bf16 v[22:25], v[172:175], v[206:209], v[22:25]
	v_mfma_f32_16x16x32_bf16 v[14:17], v[180:183], v[206:209], v[14:17]
	v_mfma_f32_16x16x32_bf16 v[6:9], v[172:175], v[214:217], v[6:9]
	v_mfma_f32_16x16x32_bf16 v[2:5], v[180:183], v[214:217], v[2:5]
	v_mfma_f32_16x16x32_bf16 v[54:57], v[176:179], v[192:195], v[54:57]
	v_mfma_f32_16x16x32_bf16 v[46:49], v[184:187], v[192:195], v[46:49]
	v_mfma_f32_16x16x32_bf16 v[38:41], v[176:179], v[202:205], v[38:41]
	v_mfma_f32_16x16x32_bf16 v[30:33], v[184:187], v[202:205], v[30:33]
	v_mfma_f32_16x16x32_bf16 v[22:25], v[176:179], v[210:213], v[22:25]
	v_mfma_f32_16x16x32_bf16 v[14:17], v[184:187], v[210:213], v[14:17]
	v_mfma_f32_16x16x32_bf16 v[6:9], v[176:179], v[218:221], v[6:9]
	v_mfma_f32_16x16x32_bf16 v[2:5], v[184:187], v[218:221], v[2:5]
	s_setprio 0
	s_barrier
	s_add_u32 s13, s13, 0x100
	s_addc_u32 s15, s15, 0
	s_cmp_ge_i32 s19, s2
	s_mov_b64 s[22:23], s[6:7]
	s_mov_b32 s18, s19
	s_cbranch_scc1 .Lpeel_exit_2525
